# stack: in-proj rotary epilogue table fetch hoisted + counted waits; out-proj bf16 residual rows prefetched; compression-bias loop software pipelined; moe-up no setprio raise
# speedup vs baseline: 1.0010x; 1.0010x over previous
; __device__ __forceinline__ void phase_prologue(const Args& a, LAS unsigned char* lds, int tid, int wid, int lane) {
;     ...
;     if (blockIdx.x < 32) {
;         const int l = blockIdx.x >> 4, kv = (blockIdx.x >> 3) & 1, ng = blockIdx.x & 7, n = ng * 64 + lane;
;         const float* pos = a.in[kv ? I_CV_POS : I_CK_POS] + (size_t)l * 4096;
;         const float* w1 = a.in[kv ? I_CV_W1 : I_CK_W1] + (size_t)l * 4096 * 512;
;         float s = 0.f;
;         for (int k = wid * 512; k < wid * 512 + 512; ++k) s += pos[k] * w1[(size_t)k * 512 + n];
.LBB0_1532:
	s_or_b64 exec, exec, s[10:11]
	s_lshl_b32 s1, s78, 6
	v_writelane_b32 v250, s1, 59
	s_cmp_lt_u32 s78, 32
	s_cbranch_scc0 .LBB0_1538
	s_lshr_b32 s2, s78, 4
	v_readlane_b32 s1, v250, 59
	s_mov_b32 s3, 0
	v_readlane_b32 s12, v250, 2
	v_readlane_b32 s36, v250, 18
	s_bfe_u32 s8, s78, 0x10003
	s_and_b32 s9, s1, 0x1c0
	s_lshl_b64 s[4:5], s[2:3], 14
	v_readlane_b32 s13, v250, 3
	v_readlane_b32 s37, v250, 19
	s_cmp_eq_u32 s8, 0
	v_readlane_b32 s14, v250, 4
	v_readlane_b32 s15, v250, 5
	v_readlane_b32 s16, v250, 6
	v_readlane_b32 s17, v250, 7
	v_readlane_b32 s20, v250, 10
	v_readlane_b32 s21, v250, 11
	v_readlane_b32 s22, v250, 12
	v_readlane_b32 s23, v250, 13
	v_readlane_b32 s26, v250, 16
	v_readlane_b32 s27, v250, 17
	s_mov_b64 s[12:13], s[36:37]
	s_cselect_b32 s14, s21, s27
	s_cselect_b32 s15, s20, s26
	s_cselect_b32 s16, s23, s13
	s_cselect_b32 s17, s22, s12
	s_lshl_b64 s[6:7], s[2:3], 23
	s_ashr_i32 s3, s84, 6
	s_lshl_b32 s10, s3, 9
	s_ashr_i32 s11, s10, 31
	s_lshl_b64 s[12:13], s[10:11], 11
	s_add_u32 s6, s6, s12
	s_addc_u32 s7, s7, s13
	v_or_b32_e32 v4, s9, v10
	s_add_u32 s6, s17, s6
	v_lshlrev_b32_e32 v0, 2, v4
	v_mov_b32_e32 v1, 0
	s_addc_u32 s7, s16, s7
	v_lshl_add_u64 v[2:3], s[6:7], 0, v[0:1]
	s_lshl_b64 s[6:7], s[10:11], 2
	s_add_u32 s4, s4, s6
	s_addc_u32 s5, s5, s7
	s_add_u32 s4, s15, s4
	s_addc_u32 s5, s14, s5
	s_add_u32 s4, s4, 60
	s_addc_u32 s5, s5, 0
	s_mov_b64 s[6:7], 0
	s_movk_i32 s9, 0x1000
	s_movk_i32 s10, 0x2000
	s_movk_i32 s11, 0x3000
	s_movk_i32 s12, 0x4000
	s_movk_i32 s13, 0x5000
	s_movk_i32 s14, 0x6000
	s_movk_i32 s15, 0x7000
	v_mov_b32_e32 v0, 0
	v_readlane_b32 s18, v250, 8
	v_readlane_b32 s19, v250, 9
	v_readlane_b32 s24, v250, 14
	v_readlane_b32 s25, v250, 15
	v_readlane_b32 s38, v250, 20
	v_readlane_b32 s39, v250, 21
	v_readlane_b32 s40, v250, 22
	v_readlane_b32 s41, v250, 23
	v_readlane_b32 s42, v250, 24
	v_readlane_b32 s43, v250, 25
	v_readlane_b32 s44, v250, 26
	v_readlane_b32 s45, v250, 27
	v_readlane_b32 s46, v250, 28
	v_readlane_b32 s47, v250, 29
	v_readlane_b32 s48, v250, 30
	v_readlane_b32 s49, v250, 31
	v_readlane_b32 s50, v250, 32
	v_readlane_b32 s51, v250, 33
	v_readfirstlane_b32 s60, v2
	v_readfirstlane_b32 s61, v3
	s_nop 4
	v_subrev_u32_e32 v186, s60, v2
	s_add_u32 s60, s60, 0x1000
	s_addc_u32 s61, s61, 0
	s_mov_b32 s64, 0
	global_load_dwordx4 v[204:207], v1, s[4:5] offset:-60
	global_load_dwordx4 v[208:211], v1, s[4:5] offset:-44
	global_load_dwordx4 v[212:215], v1, s[4:5] offset:-28
	global_load_dwordx4 v[216:219], v1, s[4:5] offset:-12
	global_load_dword v188, v186, s[60:61] offset:-4096
	global_load_dword v189, v186, s[60:61] offset:-2048
	global_load_dword v190, v186, s[60:61]
	global_load_dword v191, v186, s[60:61] offset:2048
	s_add_u32 s60, s60, 0x2000
	s_addc_u32 s61, s61, 0
	global_load_dword v192, v186, s[60:61] offset:-4096
	global_load_dword v193, v186, s[60:61] offset:-2048
	global_load_dword v194, v186, s[60:61]
	global_load_dword v195, v186, s[60:61] offset:2048
	s_add_u32 s60, s60, 0x2000
	s_addc_u32 s61, s61, 0
	global_load_dword v196, v186, s[60:61] offset:-4096
	global_load_dword v197, v186, s[60:61] offset:-2048
	global_load_dword v198, v186, s[60:61]
	global_load_dword v199, v186, s[60:61] offset:2048
	s_add_u32 s60, s60, 0x2000
	s_addc_u32 s61, s61, 0
	global_load_dword v200, v186, s[60:61] offset:-4096
	global_load_dword v201, v186, s[60:61] offset:-2048
	global_load_dword v202, v186, s[60:61]
	global_load_dword v203, v186, s[60:61] offset:2048
	s_add_u32 s60, s60, 0x2000
	s_addc_u32 s61, s61, 0
	s_add_u32 s4, s4, 64
	s_addc_u32 s5, s5, 0
	global_load_dwordx4 v[236:239], v1, s[4:5] offset:-60
	global_load_dwordx4 v[240:243], v1, s[4:5] offset:-44
	global_load_dwordx4 v[244:247], v1, s[4:5] offset:-28
	global_load_dwordx4 v[164:167], v1, s[4:5] offset:-12
	global_load_dword v220, v186, s[60:61] offset:-4096
	global_load_dword v221, v186, s[60:61] offset:-2048
	global_load_dword v222, v186, s[60:61]
	global_load_dword v223, v186, s[60:61] offset:2048
	s_add_u32 s60, s60, 0x2000
	s_addc_u32 s61, s61, 0
	global_load_dword v224, v186, s[60:61] offset:-4096
	global_load_dword v225, v186, s[60:61] offset:-2048
	global_load_dword v226, v186, s[60:61]
	global_load_dword v227, v186, s[60:61] offset:2048
	s_add_u32 s60, s60, 0x2000
	s_addc_u32 s61, s61, 0
	global_load_dword v228, v186, s[60:61] offset:-4096
	global_load_dword v229, v186, s[60:61] offset:-2048
	global_load_dword v230, v186, s[60:61]
	global_load_dword v231, v186, s[60:61] offset:2048
	s_add_u32 s60, s60, 0x2000
	s_addc_u32 s61, s61, 0
	global_load_dword v232, v186, s[60:61] offset:-4096
	global_load_dword v233, v186, s[60:61] offset:-2048
	global_load_dword v234, v186, s[60:61]
	global_load_dword v235, v186, s[60:61] offset:2048
	s_add_u32 s60, s60, 0x2000
	s_addc_u32 s61, s61, 0
	s_add_u32 s4, s4, 64
	s_addc_u32 s5, s5, 0
; __device__ __forceinline__ void phase_prologue(const Args& a, LAS unsigned char* lds, int tid, int wid, int lane) {
;     ...
;         for (int k = wid * 512; k < wid * 512 + 512; ++k) s += pos[k] * w1[(size_t)k * 512 + n];
.Lcb_loop:
	global_load_dwordx4 v[28:31], v1, s[4:5] offset:-60
	global_load_dwordx4 v[32:35], v1, s[4:5] offset:-44
	global_load_dwordx4 v[168:171], v1, s[4:5] offset:-28
	global_load_dwordx4 v[180:183], v1, s[4:5] offset:-12
	global_load_dword v11, v186, s[60:61] offset:-4096
	global_load_dword v12, v186, s[60:61] offset:-2048
	global_load_dword v13, v186, s[60:61]
	global_load_dword v14, v186, s[60:61] offset:2048
	s_add_u32 s60, s60, 0x2000
	s_addc_u32 s61, s61, 0
	global_load_dword v15, v186, s[60:61] offset:-4096
	global_load_dword v16, v186, s[60:61] offset:-2048
	global_load_dword v17, v186, s[60:61]
	global_load_dword v18, v186, s[60:61] offset:2048
	s_add_u32 s60, s60, 0x2000
	s_addc_u32 s61, s61, 0
	global_load_dword v19, v186, s[60:61] offset:-4096
	global_load_dword v20, v186, s[60:61] offset:-2048
	global_load_dword v21, v186, s[60:61]
	global_load_dword v22, v186, s[60:61] offset:2048
	s_add_u32 s60, s60, 0x2000
	s_addc_u32 s61, s61, 0
	global_load_dword v23, v186, s[60:61] offset:-4096
	global_load_dword v24, v186, s[60:61] offset:-2048
	global_load_dword v25, v186, s[60:61]
	global_load_dword v26, v186, s[60:61] offset:2048
	s_add_u32 s60, s60, 0x2000
	s_addc_u32 s61, s61, 0
	s_add_u32 s4, s4, 64
	s_addc_u32 s5, s5, 0
	s_waitcnt vmcnt(40)
	v_fmac_f32_e32 v0, v204, v188
	v_fmac_f32_e32 v0, v205, v189
	v_fmac_f32_e32 v0, v206, v190
	v_fmac_f32_e32 v0, v207, v191
	v_fmac_f32_e32 v0, v208, v192
	v_fmac_f32_e32 v0, v209, v193
	v_fmac_f32_e32 v0, v210, v194
	v_fmac_f32_e32 v0, v211, v195
	v_fmac_f32_e32 v0, v212, v196
	v_fmac_f32_e32 v0, v213, v197
	v_fmac_f32_e32 v0, v214, v198
	v_fmac_f32_e32 v0, v215, v199
	v_fmac_f32_e32 v0, v216, v200
	v_fmac_f32_e32 v0, v217, v201
	v_fmac_f32_e32 v0, v218, v202
	v_fmac_f32_e32 v0, v219, v203
	global_load_dwordx4 v[204:207], v1, s[4:5] offset:-60
	global_load_dwordx4 v[208:211], v1, s[4:5] offset:-44
	global_load_dwordx4 v[212:215], v1, s[4:5] offset:-28
	global_load_dwordx4 v[216:219], v1, s[4:5] offset:-12
	global_load_dword v188, v186, s[60:61] offset:-4096
	global_load_dword v189, v186, s[60:61] offset:-2048
	global_load_dword v190, v186, s[60:61]
	global_load_dword v191, v186, s[60:61] offset:2048
	s_add_u32 s60, s60, 0x2000
	s_addc_u32 s61, s61, 0
	global_load_dword v192, v186, s[60:61] offset:-4096
	global_load_dword v193, v186, s[60:61] offset:-2048
	global_load_dword v194, v186, s[60:61]
	global_load_dword v195, v186, s[60:61] offset:2048
	s_add_u32 s60, s60, 0x2000
	s_addc_u32 s61, s61, 0
	global_load_dword v196, v186, s[60:61] offset:-4096
	global_load_dword v197, v186, s[60:61] offset:-2048
	global_load_dword v198, v186, s[60:61]
	global_load_dword v199, v186, s[60:61] offset:2048
	s_add_u32 s60, s60, 0x2000
	s_addc_u32 s61, s61, 0
	global_load_dword v200, v186, s[60:61] offset:-4096
	global_load_dword v201, v186, s[60:61] offset:-2048
	global_load_dword v202, v186, s[60:61]
	global_load_dword v203, v186, s[60:61] offset:2048
	s_add_u32 s60, s60, 0x2000
	s_addc_u32 s61, s61, 0
	s_add_u32 s4, s4, 64
	s_addc_u32 s5, s5, 0
	s_waitcnt vmcnt(40)
	v_fmac_f32_e32 v0, v236, v220
	v_fmac_f32_e32 v0, v237, v221
	v_fmac_f32_e32 v0, v238, v222
	v_fmac_f32_e32 v0, v239, v223
	v_fmac_f32_e32 v0, v240, v224
	v_fmac_f32_e32 v0, v241, v225
	v_fmac_f32_e32 v0, v242, v226
	v_fmac_f32_e32 v0, v243, v227
	v_fmac_f32_e32 v0, v244, v228
	v_fmac_f32_e32 v0, v245, v229
	v_fmac_f32_e32 v0, v246, v230
	v_fmac_f32_e32 v0, v247, v231
	v_fmac_f32_e32 v0, v164, v232
	v_fmac_f32_e32 v0, v165, v233
	v_fmac_f32_e32 v0, v166, v234
	v_fmac_f32_e32 v0, v167, v235
	global_load_dwordx4 v[236:239], v1, s[4:5] offset:-60
	global_load_dwordx4 v[240:243], v1, s[4:5] offset:-44
	global_load_dwordx4 v[244:247], v1, s[4:5] offset:-28
	global_load_dwordx4 v[164:167], v1, s[4:5] offset:-12
	global_load_dword v220, v186, s[60:61] offset:-4096
	global_load_dword v221, v186, s[60:61] offset:-2048
	global_load_dword v222, v186, s[60:61]
	global_load_dword v223, v186, s[60:61] offset:2048
	s_add_u32 s60, s60, 0x2000
	s_addc_u32 s61, s61, 0
	global_load_dword v224, v186, s[60:61] offset:-4096
	global_load_dword v225, v186, s[60:61] offset:-2048
	global_load_dword v226, v186, s[60:61]
	global_load_dword v227, v186, s[60:61] offset:2048
	s_add_u32 s60, s60, 0x2000
	s_addc_u32 s61, s61, 0
	global_load_dword v228, v186, s[60:61] offset:-4096
	global_load_dword v229, v186, s[60:61] offset:-2048
	global_load_dword v230, v186, s[60:61]
	global_load_dword v231, v186, s[60:61] offset:2048
	s_add_u32 s60, s60, 0x2000
	s_addc_u32 s61, s61, 0
	global_load_dword v232, v186, s[60:61] offset:-4096
	global_load_dword v233, v186, s[60:61] offset:-2048
	global_load_dword v234, v186, s[60:61]
	global_load_dword v235, v186, s[60:61] offset:2048
	s_add_u32 s60, s60, 0x2000
	s_addc_u32 s61, s61, 0
	s_add_u32 s4, s4, 64
	s_addc_u32 s5, s5, 0
	s_waitcnt vmcnt(40)
	v_fmac_f32_e32 v0, v28, v11
	v_fmac_f32_e32 v0, v29, v12
	v_fmac_f32_e32 v0, v30, v13
	v_fmac_f32_e32 v0, v31, v14
	v_fmac_f32_e32 v0, v32, v15
	v_fmac_f32_e32 v0, v33, v16
	v_fmac_f32_e32 v0, v34, v17
	v_fmac_f32_e32 v0, v35, v18
	v_fmac_f32_e32 v0, v168, v19
	v_fmac_f32_e32 v0, v169, v20
	v_fmac_f32_e32 v0, v170, v21
	v_fmac_f32_e32 v0, v171, v22
	v_fmac_f32_e32 v0, v180, v23
	v_fmac_f32_e32 v0, v181, v24
	v_fmac_f32_e32 v0, v182, v25
	v_fmac_f32_e32 v0, v183, v26
	s_add_u32 s64, s64, 3
	s_cmp_lt_u32 s64, 30
	s_cbranch_scc1 .Lcb_loop
; #define LAS __attribute__((address_space(3)))
; __device__ __forceinline__ void phase_prologue(const Args& a, LAS unsigned char* lds, int tid, int wid, int lane) {
;     ...
;         for (int k = wid * 512; k < wid * 512 + 512; ++k) s += pos[k] * w1[(size_t)k * 512 + n];
;         LAS float* part = (LAS float*)(lds + 8 * 16384);
;         part[wid * 64 + lane] = s;
;         __syncthreads();
;         if (wid == 0) { float tsum = 0.f;
; #pragma unroll
;             for (int w = 0; w < 8; ++w) tsum += part[w * 64 + lane];
;             ((float*)(a.ws + WS_CBIAS))[(l * 2 + kv) * 512 + n] = tsum; }
	s_waitcnt vmcnt(20)
	v_fmac_f32_e32 v0, v204, v188
	v_fmac_f32_e32 v0, v205, v189
	v_fmac_f32_e32 v0, v206, v190
	v_fmac_f32_e32 v0, v207, v191
	v_fmac_f32_e32 v0, v208, v192
	v_fmac_f32_e32 v0, v209, v193
	v_fmac_f32_e32 v0, v210, v194
	v_fmac_f32_e32 v0, v211, v195
	v_fmac_f32_e32 v0, v212, v196
	v_fmac_f32_e32 v0, v213, v197
	v_fmac_f32_e32 v0, v214, v198
	v_fmac_f32_e32 v0, v215, v199
	v_fmac_f32_e32 v0, v216, v200
	v_fmac_f32_e32 v0, v217, v201
	v_fmac_f32_e32 v0, v218, v202
	v_fmac_f32_e32 v0, v219, v203
	s_waitcnt vmcnt(0)
	v_fmac_f32_e32 v0, v236, v220
	v_fmac_f32_e32 v0, v237, v221
	v_fmac_f32_e32 v0, v238, v222
	v_fmac_f32_e32 v0, v239, v223
	v_fmac_f32_e32 v0, v240, v224
	v_fmac_f32_e32 v0, v241, v225
	v_fmac_f32_e32 v0, v242, v226
	v_fmac_f32_e32 v0, v243, v227
	v_fmac_f32_e32 v0, v244, v228
	v_fmac_f32_e32 v0, v245, v229
	v_fmac_f32_e32 v0, v246, v230
	v_fmac_f32_e32 v0, v247, v231
	v_fmac_f32_e32 v0, v164, v232
	v_fmac_f32_e32 v0, v165, v233
	v_fmac_f32_e32 v0, v166, v234
	v_fmac_f32_e32 v0, v167, v235
	s_lshl_b32 s3, s3, 8
	s_add_i32 s3, s3, 0
	v_lshl_add_u32 v1, v10, 2, s3
	v_add_u32_e32 v1, 0x20000, v1
	s_cmp_gt_u32 s84, 63
	ds_write_b32 v1, v0
	s_waitcnt lgkmcnt(0)
	s_barrier
	s_cbranch_scc1 .LBB0_1537
	v_lshl_add_u32 v0, v10, 2, 0
	v_add_u32_e32 v5, 0x20000, v0
	ds_read2st64_b32 v[0:1], v5 offset1:1
	ds_read2st64_b32 v[2:3], v5 offset0:2 offset1:3
	ds_read2st64_b32 v[6:7], v5 offset0:4 offset1:5
	ds_read2st64_b32 v[8:9], v5 offset0:6 offset1:7
	s_lshl_b32 s2, s2, 10
	s_lshl_b32 s3, s8, 9
	s_or_b32 s2, s3, s2
	s_waitcnt lgkmcnt(3)
	v_add_f32_e32 v0, 0, v0
	v_add_f32_e32 v0, v0, v1
	s_waitcnt lgkmcnt(2)
	v_add_f32_e32 v0, v0, v2
	v_add_f32_e32 v0, v0, v3
	s_waitcnt lgkmcnt(1)
	v_add_f32_e32 v0, v0, v6
	v_add_f32_e32 v0, v0, v7
	s_waitcnt lgkmcnt(0)
	v_add_f32_e32 v0, v0, v8
	v_add_f32_e32 v2, v0, v9
	v_or_b32_e32 v0, s2, v4
	v_mov_b32_e32 v1, 0
	v_lshl_add_u64 v[0:1], v[0:1], 2, s[80:81]
	v_add_co_u32_e32 v0, vcc, 0x32680000, v0
	s_nop 1
	v_addc_co_u32_e32 v1, vcc, 0, v1, vcc
	global_store_dword v[0:1], v2, off

;     __device__ __forceinline__ void operator()(const f32x4 (&acc)[2][2][4][2], const Unit& u, int wr, int wc, int fr, int fq) const {
;     ...
;                 for (int m = 0; m < 4; ++m) { const int t = row0 + ai * HALF + m * 16, b = t >> 11, s = t & 2047;
;                     const float rsc = scale * rr8[ai][m];
;                     const f32x4 c = *(const f32x4*)(cosN + s * 64 + 4 * uu) * rsc, sn = *(const f32x4*)(sinN + s * 64 + 4 * uu) * rsc;
.LBB0_1968:
	s_andn2_b64 vcc, exec, s[24:25]
	s_cbranch_vccnz .LBB0_2034
	v_and_b32_e32 v13, 0x7cf, v12
	v_lshlrev_b32_e32 v2, 8, v13
	v_lshl_add_u64 v[4:5], v[166:167], 0, v[2:3]
	v_lshl_add_u64 v[8:9], v[168:169], 0, v[2:3]
	global_load_dwordx4 v[4:7], v[4:5], off
	v_lshlrev_b32_e32 v2, 7, v13
	global_load_dwordx4 v[8:11], v[8:9], off
	v_lshlrev_b32_e32 v248, 8, v13
	v_mov_b32_e32 v249, v3
	v_lshl_add_u64 v[246:247], v[166:167], 0, v[248:249]
	v_lshl_add_u64 v[248:249], v[168:169], 0, v[248:249]
	s_mov_b64 s[100:101], 0x1000
	v_lshl_add_u64 v[198:199], s[100:101], 0, v[246:247]
	global_load_dwordx4 v[210:213], v[198:199], off
	v_lshl_add_u64 v[198:199], s[100:101], 0, v[248:249]
	global_load_dwordx4 v[206:209], v[198:199], off
	s_mov_b64 s[100:101], 0x2000
	v_lshl_add_u64 v[198:199], s[100:101], 0, v[246:247]
	global_load_dwordx4 v[218:221], v[198:199], off
	v_lshl_add_u64 v[198:199], s[100:101], 0, v[248:249]
	global_load_dwordx4 v[214:217], v[198:199], off
	s_mov_b64 s[100:101], 0x3000
	v_lshl_add_u64 v[198:199], s[100:101], 0, v[246:247]
	global_load_dwordx4 v[226:229], v[198:199], off
	v_lshl_add_u64 v[198:199], s[100:101], 0, v[248:249]
	global_load_dwordx4 v[222:225], v[198:199], off
	s_mov_b64 s[100:101], 0x8000
	v_lshl_add_u64 v[198:199], s[100:101], 0, v[246:247]
	global_load_dwordx4 v[234:237], v[198:199], off
	v_lshl_add_u64 v[198:199], s[100:101], 0, v[248:249]
	global_load_dwordx4 v[230:233], v[198:199], off
	s_mov_b64 s[100:101], 0x9000
	v_lshl_add_u64 v[198:199], s[100:101], 0, v[246:247]
	global_load_dwordx4 v[242:245], v[198:199], off
	v_lshl_add_u64 v[198:199], s[100:101], 0, v[248:249]
	global_load_dwordx4 v[238:241], v[198:199], off
	s_mov_b64 s[30:31], -1
	s_and_b64 vcc, exec, s[28:29]
	s_mul_hi_u32 s17, s19, 0x802000
	s_mul_i32 s19, s19, 0x802000
	v_lshlrev_b32_e32 v170, 1, v2
	s_cbranch_vccz .LBB0_1971
	s_add_u32 s30, s45, s19
	s_addc_u32 s31, s46, s17
	s_ashr_i32 s27, s26, 31
	s_lshl_b64 s[24:25], s[26:27], 19
	s_add_u32 s24, s30, s24
	s_addc_u32 s25, s31, s25
	v_mov_b32_e32 v171, v3
	v_lshl_add_u64 v[178:179], s[24:25], 0, v[170:171]
	s_mov_b64 s[30:31], 0

; __device__ __forceinline__ unsigned cvtpk(float lo, float hi) { unsigned r; asm volatile("v_cvt_pk_bf16_f32 %0, %1, %2" : "=v"(r) : "v"(lo), "v"(hi)); return r; }
;     __device__ __forceinline__ void operator()(const f32x4 (&acc)[2][2][4][2], const Unit& u, int wr, int wc, int fr, int fq) const {
;     ...
;                     const f32x4 c = *(const f32x4*)(cosN + s * 64 + 4 * uu) * rsc, sn = *(const f32x4*)(sinN + s * 64 + 4 * uu) * rsc;
; #pragma unroll
;                     for (int bj = 0; bj < 2; ++bj) { const f32x4 x1 = acc[ai][bj][m][0], x2 = acc[ai][bj][m][1];
;                         const f32x4 o1 = x1 * c - x2 * sn, o2 = x1 * sn + x2 * c;
;                         bf16_t* dst = isq ? (QN + (size_t)t * 1024 + (2 * pn + bj) * 128 + 4 * uu) : (KV6 + (size_t)(pn - 4) * kvstride + ((size_t)(b * 2 + bj) * 2048 + s) * 128 + 4 * uu);
;                         u32x2 w1, w2; w1.x = cvtpk(o1[0], o1[1]); w1.y = cvtpk(o1[2], o1[3]); w2.x = cvtpk(o2[0], o2[1]); w2.y = cvtpk(o2[2], o2[3]);
;                         *(u32x2*)dst = w1; *(u32x2*)(dst + 64) = w2; } }
.LBB0_1973:
	v_mov_b32_e32 v2, 0x3db504f3
	v_cndmask_b32_e64 v13, 1.0, v2, s[4:5]
	s_waitcnt vmcnt(12)
	v_mul_f32_e32 v2, v13, v30
	s_waitcnt vmcnt(10)
	v_pk_mul_f32 v[8:9], v[2:3], v[8:9] op_sel_hi:[0,1]
	v_pk_mul_f32 v[4:5], v[2:3], v[4:5] op_sel_hi:[0,1]
	v_pk_mul_f32 v[10:11], v[2:3], v[10:11] op_sel_hi:[0,1]
	v_pk_mul_f32 v[172:173], v[156:157], v[8:9]
	v_pk_mul_f32 v[6:7], v[2:3], v[6:7] op_sel_hi:[0,1]
	v_pk_mul_f32 v[174:175], v[158:159], v[10:11]
	v_pk_fma_f32 v[172:173], v[160:161], v[4:5], v[172:173] neg_lo:[0,0,1] neg_hi:[0,0,1]
	v_lshlrev_b32_e32 v2, 1, v0
	v_cndmask_b32_e64 v15, 0, 1, s[28:29]
	v_pk_fma_f32 v[174:175], v[162:163], v[6:7], v[174:175] neg_lo:[0,0,1] neg_hi:[0,0,1]
	v_pk_mul_f32 v[186:187], v[160:161], v[8:9]
	v_pk_mul_f32 v[196:197], v[162:163], v[10:11]
	v_lshl_add_u64 v[178:179], v[178:179], 0, v[2:3]
	v_cvt_pk_bf16_f32 v172, v172, v173
	v_cvt_pk_bf16_f32 v173, v174, v175
	v_cmp_ne_u32_e64 s[4:5], 1, v15
	s_andn2_b64 vcc, exec, s[28:29]
	s_mov_b64 s[28:29], -1
	v_pk_fma_f32 v[196:197], v[158:159], v[6:7], v[196:197]
	v_pk_fma_f32 v[186:187], v[156:157], v[4:5], v[186:187]
	s_nop 0
	v_cvt_pk_bf16_f32 v174, v186, v187
	v_cvt_pk_bf16_f32 v175, v196, v197
	global_store_dwordx2 v[178:179], v[172:173], off
	global_store_dwordx2 v[178:179], v[174:175], off offset:128
	s_cbranch_vccnz .LBB0_1975
	s_add_u32 s25, s45, s19
	s_addc_u32 s27, s46, s17
	s_or_b32 s28, s59, 1
	s_ashr_i32 s29, s28, 31
	s_lshl_b64 s[28:29], s[28:29], 19
	s_add_u32 s28, s25, s28
	s_addc_u32 s29, s27, s29
	v_mov_b32_e32 v171, v3
	v_lshl_add_u64 v[178:179], s[28:29], 0, v[170:171]
	s_mov_b64 s[28:29], 0

; __device__ __forceinline__ unsigned cvtpk(float lo, float hi) { unsigned r; asm volatile("v_cvt_pk_bf16_f32 %0, %1, %2" : "=v"(r) : "v"(lo), "v"(hi)); return r; }
;     __device__ __forceinline__ void operator()(const f32x4 (&acc)[2][2][4][2], const Unit& u, int wr, int wc, int fr, int fq) const {
;     ...
;                     const f32x4 c = *(const f32x4*)(cosN + s * 64 + 4 * uu) * rsc, sn = *(const f32x4*)(sinN + s * 64 + 4 * uu) * rsc;
; #pragma unroll
;                     for (int bj = 0; bj < 2; ++bj) { const f32x4 x1 = acc[ai][bj][m][0], x2 = acc[ai][bj][m][1];
;                         const f32x4 o1 = x1 * c - x2 * sn, o2 = x1 * sn + x2 * c;
;                         bf16_t* dst = isq ? (QN + (size_t)t * 1024 + (2 * pn + bj) * 128 + 4 * uu) : (KV6 + (size_t)(pn - 4) * kvstride + ((size_t)(b * 2 + bj) * 2048 + s) * 128 + 4 * uu);
;                         u32x2 w1, w2; w1.x = cvtpk(o1[0], o1[1]); w1.y = cvtpk(o1[2], o1[3]); w2.x = cvtpk(o2[0], o2[1]); w2.y = cvtpk(o2[2], o2[3]);
;                         *(u32x2*)dst = w1; *(u32x2*)(dst + 64) = w2; } }
.LBB0_1977:
	v_pk_mul_f32 v[172:173], v[144:145], v[8:9]
	v_pk_mul_f32 v[8:9], v[152:153], v[8:9]
	v_pk_mul_f32 v[170:171], v[146:147], v[10:11]
	v_pk_fma_f32 v[172:173], v[152:153], v[4:5], v[172:173] neg_lo:[0,0,1] neg_hi:[0,0,1]
	v_pk_mul_f32 v[10:11], v[154:155], v[10:11]
	v_pk_fma_f32 v[4:5], v[144:145], v[4:5], v[8:9]
	s_movk_i32 s25, 0x7df
	v_pk_fma_f32 v[170:171], v[154:155], v[6:7], v[170:171] neg_lo:[0,0,1] neg_hi:[0,0,1]
	v_pk_fma_f32 v[6:7], v[146:147], v[6:7], v[10:11]
	v_lshl_add_u64 v[8:9], v[178:179], 0, v[2:3]
	v_cvt_pk_bf16_f32 v10, v172, v173
	v_cvt_pk_bf16_f32 v11, v170, v171
	v_cvt_pk_bf16_f32 v4, v4, v5
	v_cvt_pk_bf16_f32 v5, v6, v7
	v_bitop3_b32 v15, v12, s25, 16 bitop3:0xc8
	global_store_dwordx2 v[8:9], v[10:11], off
	global_store_dwordx2 v[8:9], v[4:5], off offset:128
	v_lshlrev_b32_e32 v4, 8, v15
	v_mov_b32_e32 v5, v3
	v_lshl_add_u64 v[6:7], v[166:167], 0, v[4:5]
	v_lshl_add_u64 v[4:5], v[168:169], 0, v[4:5]
	s_nop 0
	v_lshlrev_b32_e32 v15, 7, v15
	s_mov_b64 s[28:29], -1
	s_and_b64 vcc, exec, s[4:5]
	v_lshlrev_b32_e32 v170, 1, v15
	s_cbranch_vccnz .LBB0_1979
	s_add_u32 s25, s45, s19
	s_addc_u32 s30, s46, s17
	s_ashr_i32 s27, s26, 31
	s_lshl_b64 s[28:29], s[26:27], 19
	s_add_u32 s28, s25, s28
	s_addc_u32 s29, s30, s29
	v_mov_b32_e32 v171, v3
	v_lshl_add_u64 v[178:179], s[28:29], 0, v[170:171]
	s_mov_b64 s[28:29], 0

; __device__ __forceinline__ unsigned cvtpk(float lo, float hi) { unsigned r; asm volatile("v_cvt_pk_bf16_f32 %0, %1, %2" : "=v"(r) : "v"(lo), "v"(hi)); return r; }
;     __device__ __forceinline__ void operator()(const f32x4 (&acc)[2][2][4][2], const Unit& u, int wr, int wc, int fr, int fq) const {
;     ...
;                     const float rsc = scale * rr8[ai][m];
;                     const f32x4 c = *(const f32x4*)(cosN + s * 64 + 4 * uu) * rsc, sn = *(const f32x4*)(sinN + s * 64 + 4 * uu) * rsc;
; #pragma unroll
;                     for (int bj = 0; bj < 2; ++bj) { const f32x4 x1 = acc[ai][bj][m][0], x2 = acc[ai][bj][m][1];
;                         const f32x4 o1 = x1 * c - x2 * sn, o2 = x1 * sn + x2 * c;
;                         bf16_t* dst = isq ? (QN + (size_t)t * 1024 + (2 * pn + bj) * 128 + 4 * uu) : (KV6 + (size_t)(pn - 4) * kvstride + ((size_t)(b * 2 + bj) * 2048 + s) * 128 + 4 * uu);
;                         u32x2 w1, w2; w1.x = cvtpk(o1[0], o1[1]); w1.y = cvtpk(o1[2], o1[3]); w2.x = cvtpk(o2[0], o2[1]); w2.y = cvtpk(o2[2], o2[3]);
;                         *(u32x2*)dst = w1; *(u32x2*)(dst + 64) = w2; } }
.LBB0_1981:
	v_mul_f32_e32 v172, v13, v28
	s_waitcnt vmcnt(12)
	v_pk_mul_f32 v[206:207], v[172:173], v[206:207] op_sel_hi:[0,1]
	v_pk_mul_f32 v[210:211], v[172:173], v[210:211] op_sel_hi:[0,1]
	v_pk_mul_f32 v[208:209], v[172:173], v[208:209] op_sel_hi:[0,1]
	v_pk_mul_f32 v[174:175], v[140:141], v[206:207]
	v_pk_mul_f32 v[212:213], v[172:173], v[212:213] op_sel_hi:[0,1]
	v_pk_mul_f32 v[172:173], v[142:143], v[208:209]
	v_pk_fma_f32 v[174:175], v[148:149], v[210:211], v[174:175] neg_lo:[0,0,1] neg_hi:[0,0,1]
	v_pk_fma_f32 v[172:173], v[150:151], v[212:213], v[172:173] neg_lo:[0,0,1] neg_hi:[0,0,1]
	v_pk_mul_f32 v[186:187], v[150:151], v[208:209]
	v_pk_mul_f32 v[196:197], v[148:149], v[206:207]
	v_lshl_add_u64 v[178:179], v[178:179], 0, v[2:3]
	v_cvt_pk_bf16_f32 v174, v174, v175
	v_cvt_pk_bf16_f32 v175, v172, v173
	s_and_b64 vcc, exec, s[4:5]
	s_mov_b64 s[28:29], -1
	v_pk_fma_f32 v[186:187], v[142:143], v[212:213], v[186:187]
	v_pk_fma_f32 v[196:197], v[140:141], v[210:211], v[196:197]
	s_nop 0
	v_cvt_pk_bf16_f32 v172, v196, v197
	v_cvt_pk_bf16_f32 v173, v186, v187
	global_store_dwordx2 v[178:179], v[174:175], off
	global_store_dwordx2 v[178:179], v[172:173], off offset:128
	s_cbranch_vccnz .LBB0_1983
	s_add_u32 s25, s45, s19
	s_addc_u32 s27, s46, s17
	s_or_b32 s28, s59, 1
	s_ashr_i32 s29, s28, 31
	s_lshl_b64 s[28:29], s[28:29], 19
	s_add_u32 s28, s25, s28
	s_addc_u32 s29, s27, s29
	v_mov_b32_e32 v171, v3
	v_lshl_add_u64 v[178:179], s[28:29], 0, v[170:171]
	s_mov_b64 s[28:29], 0

; __device__ __forceinline__ unsigned cvtpk(float lo, float hi) { unsigned r; asm volatile("v_cvt_pk_bf16_f32 %0, %1, %2" : "=v"(r) : "v"(lo), "v"(hi)); return r; }
;     __device__ __forceinline__ void operator()(const f32x4 (&acc)[2][2][4][2], const Unit& u, int wr, int wc, int fr, int fq) const {
;     ...
;                     const f32x4 c = *(const f32x4*)(cosN + s * 64 + 4 * uu) * rsc, sn = *(const f32x4*)(sinN + s * 64 + 4 * uu) * rsc;
; #pragma unroll
;                     for (int bj = 0; bj < 2; ++bj) { const f32x4 x1 = acc[ai][bj][m][0], x2 = acc[ai][bj][m][1];
;                         const f32x4 o1 = x1 * c - x2 * sn, o2 = x1 * sn + x2 * c;
;                         bf16_t* dst = isq ? (QN + (size_t)t * 1024 + (2 * pn + bj) * 128 + 4 * uu) : (KV6 + (size_t)(pn - 4) * kvstride + ((size_t)(b * 2 + bj) * 2048 + s) * 128 + 4 * uu);
;                         u32x2 w1, w2; w1.x = cvtpk(o1[0], o1[1]); w1.y = cvtpk(o1[2], o1[3]); w2.x = cvtpk(o2[0], o2[1]); w2.y = cvtpk(o2[2], o2[3]);
;                         *(u32x2*)dst = w1; *(u32x2*)(dst + 64) = w2; } }
.LBB0_1985:
	v_pk_mul_f32 v[172:173], v[128:129], v[206:207]
	v_pk_mul_f32 v[206:207], v[136:137], v[206:207]
	v_pk_mul_f32 v[170:171], v[130:131], v[208:209]
	v_pk_mul_f32 v[208:209], v[138:139], v[208:209]
	v_pk_fma_f32 v[206:207], v[128:129], v[210:211], v[206:207]
	s_movk_i32 s25, 0x7ef
	v_pk_fma_f32 v[170:171], v[138:139], v[212:213], v[170:171] neg_lo:[0,0,1] neg_hi:[0,0,1]
	v_pk_fma_f32 v[172:173], v[136:137], v[210:211], v[172:173] neg_lo:[0,0,1] neg_hi:[0,0,1]
	v_pk_fma_f32 v[208:209], v[130:131], v[212:213], v[208:209]
	v_lshl_add_u64 v[210:211], v[178:179], 0, v[2:3]
	v_cvt_pk_bf16_f32 v212, v172, v173
	v_cvt_pk_bf16_f32 v213, v170, v171
	v_cvt_pk_bf16_f32 v206, v206, v207
	v_cvt_pk_bf16_f32 v207, v208, v209
	v_bitop3_b32 v15, v12, s25, 32 bitop3:0xc8
	global_store_dwordx2 v[210:211], v[212:213], off
	global_store_dwordx2 v[210:211], v[206:207], off offset:128
	s_mov_b64 s[100:101], 0xa000
	v_lshl_add_u64 v[198:199], s[100:101], 0, v[246:247]
	global_load_dwordx4 v[210:213], v[198:199], off
	v_lshl_add_u64 v[198:199], s[100:101], 0, v[248:249]
	global_load_dwordx4 v[206:209], v[198:199], off
	v_lshlrev_b32_e32 v4, 8, v15
	v_mov_b32_e32 v5, v3
	v_lshl_add_u64 v[6:7], v[166:167], 0, v[4:5]
	v_lshl_add_u64 v[4:5], v[168:169], 0, v[4:5]
	s_nop 0
	v_lshlrev_b32_e32 v15, 7, v15
	s_mov_b64 s[28:29], -1
	s_and_b64 vcc, exec, s[4:5]
	v_lshlrev_b32_e32 v170, 1, v15
	s_cbranch_vccnz .LBB0_1987
	s_add_u32 s25, s45, s19
	s_addc_u32 s30, s46, s17
	s_ashr_i32 s27, s26, 31
	s_lshl_b64 s[28:29], s[26:27], 19
	s_add_u32 s28, s25, s28
	s_addc_u32 s29, s30, s29
	v_mov_b32_e32 v171, v3
	v_lshl_add_u64 v[178:179], s[28:29], 0, v[170:171]
	s_mov_b64 s[28:29], 0

; __device__ __forceinline__ unsigned cvtpk(float lo, float hi) { unsigned r; asm volatile("v_cvt_pk_bf16_f32 %0, %1, %2" : "=v"(r) : "v"(lo), "v"(hi)); return r; }
;     __device__ __forceinline__ void operator()(const f32x4 (&acc)[2][2][4][2], const Unit& u, int wr, int wc, int fr, int fq) const {
;     ...
;                     const float rsc = scale * rr8[ai][m];
;                     const f32x4 c = *(const f32x4*)(cosN + s * 64 + 4 * uu) * rsc, sn = *(const f32x4*)(sinN + s * 64 + 4 * uu) * rsc;
; #pragma unroll
;                     for (int bj = 0; bj < 2; ++bj) { const f32x4 x1 = acc[ai][bj][m][0], x2 = acc[ai][bj][m][1];
;                         const f32x4 o1 = x1 * c - x2 * sn, o2 = x1 * sn + x2 * c;
;                         bf16_t* dst = isq ? (QN + (size_t)t * 1024 + (2 * pn + bj) * 128 + 4 * uu) : (KV6 + (size_t)(pn - 4) * kvstride + ((size_t)(b * 2 + bj) * 2048 + s) * 128 + 4 * uu);
;                         u32x2 w1, w2; w1.x = cvtpk(o1[0], o1[1]); w1.y = cvtpk(o1[2], o1[3]); w2.x = cvtpk(o2[0], o2[1]); w2.y = cvtpk(o2[2], o2[3]);
;                         *(u32x2*)dst = w1; *(u32x2*)(dst + 64) = w2; } }
.LBB0_1989:
	v_mul_f32_e32 v172, v13, v26
	s_waitcnt vmcnt(16)
	v_pk_mul_f32 v[214:215], v[172:173], v[214:215] op_sel_hi:[0,1]
	v_pk_mul_f32 v[218:219], v[172:173], v[218:219] op_sel_hi:[0,1]
	v_pk_mul_f32 v[216:217], v[172:173], v[216:217] op_sel_hi:[0,1]
	v_pk_mul_f32 v[174:175], v[124:125], v[214:215]
	v_pk_mul_f32 v[220:221], v[172:173], v[220:221] op_sel_hi:[0,1]
	v_pk_mul_f32 v[172:173], v[126:127], v[216:217]
	v_pk_fma_f32 v[174:175], v[132:133], v[218:219], v[174:175] neg_lo:[0,0,1] neg_hi:[0,0,1]
	v_pk_fma_f32 v[172:173], v[134:135], v[220:221], v[172:173] neg_lo:[0,0,1] neg_hi:[0,0,1]
	v_pk_mul_f32 v[186:187], v[134:135], v[216:217]
	v_pk_mul_f32 v[196:197], v[132:133], v[214:215]
	v_lshl_add_u64 v[178:179], v[178:179], 0, v[2:3]
	v_cvt_pk_bf16_f32 v174, v174, v175
	v_cvt_pk_bf16_f32 v175, v172, v173
	s_and_b64 vcc, exec, s[4:5]
	s_mov_b64 s[28:29], -1
	v_pk_fma_f32 v[186:187], v[126:127], v[220:221], v[186:187]
	v_pk_fma_f32 v[196:197], v[124:125], v[218:219], v[196:197]
	s_nop 0
	v_cvt_pk_bf16_f32 v172, v196, v197
	v_cvt_pk_bf16_f32 v173, v186, v187
	global_store_dwordx2 v[178:179], v[174:175], off
	global_store_dwordx2 v[178:179], v[172:173], off offset:128
	s_cbranch_vccnz .LBB0_1991
	s_add_u32 s25, s45, s19
	s_addc_u32 s27, s46, s17
	s_or_b32 s28, s59, 1
	s_ashr_i32 s29, s28, 31
	s_lshl_b64 s[28:29], s[28:29], 19
	s_add_u32 s28, s25, s28
	s_addc_u32 s29, s27, s29
	v_mov_b32_e32 v171, v3
	v_lshl_add_u64 v[178:179], s[28:29], 0, v[170:171]
	s_mov_b64 s[28:29], 0

; __device__ __forceinline__ unsigned cvtpk(float lo, float hi) { unsigned r; asm volatile("v_cvt_pk_bf16_f32 %0, %1, %2" : "=v"(r) : "v"(lo), "v"(hi)); return r; }
;     __device__ __forceinline__ void operator()(const f32x4 (&acc)[2][2][4][2], const Unit& u, int wr, int wc, int fr, int fq) const {
;     ...
;                     const f32x4 c = *(const f32x4*)(cosN + s * 64 + 4 * uu) * rsc, sn = *(const f32x4*)(sinN + s * 64 + 4 * uu) * rsc;
; #pragma unroll
;                     for (int bj = 0; bj < 2; ++bj) { const f32x4 x1 = acc[ai][bj][m][0], x2 = acc[ai][bj][m][1];
;                         const f32x4 o1 = x1 * c - x2 * sn, o2 = x1 * sn + x2 * c;
;                         bf16_t* dst = isq ? (QN + (size_t)t * 1024 + (2 * pn + bj) * 128 + 4 * uu) : (KV6 + (size_t)(pn - 4) * kvstride + ((size_t)(b * 2 + bj) * 2048 + s) * 128 + 4 * uu);
;                         u32x2 w1, w2; w1.x = cvtpk(o1[0], o1[1]); w1.y = cvtpk(o1[2], o1[3]); w2.x = cvtpk(o2[0], o2[1]); w2.y = cvtpk(o2[2], o2[3]);
;                         *(u32x2*)dst = w1; *(u32x2*)(dst + 64) = w2; } }
.LBB0_1993:
	v_pk_mul_f32 v[172:173], v[112:113], v[214:215]
	v_pk_mul_f32 v[214:215], v[120:121], v[214:215]
	v_pk_mul_f32 v[170:171], v[114:115], v[216:217]
	v_pk_mul_f32 v[216:217], v[122:123], v[216:217]
	v_pk_fma_f32 v[214:215], v[112:113], v[218:219], v[214:215]
	s_movk_i32 s25, 0x7ff
	v_pk_fma_f32 v[170:171], v[122:123], v[220:221], v[170:171] neg_lo:[0,0,1] neg_hi:[0,0,1]
	v_pk_fma_f32 v[172:173], v[120:121], v[218:219], v[172:173] neg_lo:[0,0,1] neg_hi:[0,0,1]
	v_pk_fma_f32 v[216:217], v[114:115], v[220:221], v[216:217]
	v_lshl_add_u64 v[218:219], v[178:179], 0, v[2:3]
	v_cvt_pk_bf16_f32 v220, v172, v173
	v_cvt_pk_bf16_f32 v221, v170, v171
	v_cvt_pk_bf16_f32 v214, v214, v215
	v_cvt_pk_bf16_f32 v215, v216, v217
	v_bitop3_b32 v15, v12, s25, 48 bitop3:0xc8
	global_store_dwordx2 v[218:219], v[220:221], off
	global_store_dwordx2 v[218:219], v[214:215], off offset:128
	s_mov_b64 s[100:101], 0xb000
	v_lshl_add_u64 v[198:199], s[100:101], 0, v[246:247]
	global_load_dwordx4 v[218:221], v[198:199], off
	v_lshl_add_u64 v[198:199], s[100:101], 0, v[248:249]
	global_load_dwordx4 v[214:217], v[198:199], off
	v_lshlrev_b32_e32 v4, 8, v15
	v_mov_b32_e32 v5, v3
	v_lshl_add_u64 v[6:7], v[166:167], 0, v[4:5]
	v_lshl_add_u64 v[4:5], v[168:169], 0, v[4:5]
	s_nop 0
	v_lshlrev_b32_e32 v15, 7, v15
	s_mov_b64 s[28:29], -1
	s_and_b64 vcc, exec, s[4:5]
	v_lshlrev_b32_e32 v170, 1, v15
	s_cbranch_vccnz .LBB0_1995
	s_add_u32 s25, s45, s19
	s_addc_u32 s28, s46, s17
	s_ashr_i32 s27, s26, 31
	s_lshl_b64 s[26:27], s[26:27], 19
	s_add_u32 s26, s25, s26
	s_addc_u32 s27, s28, s27
	v_mov_b32_e32 v171, v3
	v_lshl_add_u64 v[178:179], s[26:27], 0, v[170:171]
	s_mov_b64 s[28:29], 0

; __device__ __forceinline__ unsigned cvtpk(float lo, float hi) { unsigned r; asm volatile("v_cvt_pk_bf16_f32 %0, %1, %2" : "=v"(r) : "v"(lo), "v"(hi)); return r; }
;     __device__ __forceinline__ void operator()(const f32x4 (&acc)[2][2][4][2], const Unit& u, int wr, int wc, int fr, int fq) const {
;     ...
;                     const float rsc = scale * rr8[ai][m];
;                     const f32x4 c = *(const f32x4*)(cosN + s * 64 + 4 * uu) * rsc, sn = *(const f32x4*)(sinN + s * 64 + 4 * uu) * rsc;
; #pragma unroll
;                     for (int bj = 0; bj < 2; ++bj) { const f32x4 x1 = acc[ai][bj][m][0], x2 = acc[ai][bj][m][1];
;                         const f32x4 o1 = x1 * c - x2 * sn, o2 = x1 * sn + x2 * c;
;                         bf16_t* dst = isq ? (QN + (size_t)t * 1024 + (2 * pn + bj) * 128 + 4 * uu) : (KV6 + (size_t)(pn - 4) * kvstride + ((size_t)(b * 2 + bj) * 2048 + s) * 128 + 4 * uu);
;                         u32x2 w1, w2; w1.x = cvtpk(o1[0], o1[1]); w1.y = cvtpk(o1[2], o1[3]); w2.x = cvtpk(o2[0], o2[1]); w2.y = cvtpk(o2[2], o2[3]);
;                         *(u32x2*)dst = w1; *(u32x2*)(dst + 64) = w2; } }
.LBB0_1997:
	v_mul_f32_e32 v172, v13, v22
	s_waitcnt vmcnt(20)
	v_pk_mul_f32 v[222:223], v[172:173], v[222:223] op_sel_hi:[0,1]
	v_pk_mul_f32 v[226:227], v[172:173], v[226:227] op_sel_hi:[0,1]
	v_pk_mul_f32 v[224:225], v[172:173], v[224:225] op_sel_hi:[0,1]
	v_pk_mul_f32 v[174:175], v[108:109], v[222:223]
	v_pk_mul_f32 v[228:229], v[172:173], v[228:229] op_sel_hi:[0,1]
	v_pk_mul_f32 v[172:173], v[110:111], v[224:225]
	v_pk_fma_f32 v[174:175], v[116:117], v[226:227], v[174:175] neg_lo:[0,0,1] neg_hi:[0,0,1]
	v_pk_fma_f32 v[172:173], v[118:119], v[228:229], v[172:173] neg_lo:[0,0,1] neg_hi:[0,0,1]
	v_pk_mul_f32 v[186:187], v[118:119], v[224:225]
	v_pk_mul_f32 v[196:197], v[116:117], v[222:223]
	v_lshl_add_u64 v[178:179], v[178:179], 0, v[2:3]
	v_cvt_pk_bf16_f32 v174, v174, v175
	v_cvt_pk_bf16_f32 v175, v172, v173
	s_and_b64 vcc, exec, s[4:5]
	s_mov_b64 s[26:27], -1
	v_pk_fma_f32 v[186:187], v[110:111], v[228:229], v[186:187]
	v_pk_fma_f32 v[196:197], v[108:109], v[226:227], v[196:197]
	s_nop 0
	v_cvt_pk_bf16_f32 v172, v196, v197
	v_cvt_pk_bf16_f32 v173, v186, v187
	global_store_dwordx2 v[178:179], v[174:175], off
	global_store_dwordx2 v[178:179], v[172:173], off offset:128
	s_cbranch_vccnz .LBB0_1999
	s_add_u32 s25, s45, s19
	s_addc_u32 s28, s46, s17
	s_or_b32 s26, s59, 1
	s_ashr_i32 s27, s26, 31
	s_lshl_b64 s[26:27], s[26:27], 19
	s_add_u32 s26, s25, s26
	s_addc_u32 s27, s28, s27
	v_mov_b32_e32 v171, v3
	v_lshl_add_u64 v[178:179], s[26:27], 0, v[170:171]
	s_mov_b64 s[26:27], 0

; __device__ __forceinline__ unsigned cvtpk(float lo, float hi) { unsigned r; asm volatile("v_cvt_pk_bf16_f32 %0, %1, %2" : "=v"(r) : "v"(lo), "v"(hi)); return r; }
;     __device__ __forceinline__ void operator()(const f32x4 (&acc)[2][2][4][2], const Unit& u, int wr, int wc, int fr, int fq) const {
;     ...
;                     const f32x4 c = *(const f32x4*)(cosN + s * 64 + 4 * uu) * rsc, sn = *(const f32x4*)(sinN + s * 64 + 4 * uu) * rsc;
; #pragma unroll
;                     for (int bj = 0; bj < 2; ++bj) { const f32x4 x1 = acc[ai][bj][m][0], x2 = acc[ai][bj][m][1];
;                         const f32x4 o1 = x1 * c - x2 * sn, o2 = x1 * sn + x2 * c;
;                         bf16_t* dst = isq ? (QN + (size_t)t * 1024 + (2 * pn + bj) * 128 + 4 * uu) : (KV6 + (size_t)(pn - 4) * kvstride + ((size_t)(b * 2 + bj) * 2048 + s) * 128 + 4 * uu);
;                         u32x2 w1, w2; w1.x = cvtpk(o1[0], o1[1]); w1.y = cvtpk(o1[2], o1[3]); w2.x = cvtpk(o2[0], o2[1]); w2.y = cvtpk(o2[2], o2[3]);
;                         *(u32x2*)dst = w1; *(u32x2*)(dst + 64) = w2; } }
.LBB0_2001:
	v_pk_mul_f32 v[172:173], v[100:101], v[222:223]
	v_pk_mul_f32 v[222:223], v[104:105], v[222:223]
	v_pk_mul_f32 v[170:171], v[102:103], v[224:225]
	v_pk_mul_f32 v[224:225], v[106:107], v[224:225]
	v_pk_fma_f32 v[222:223], v[100:101], v[226:227], v[222:223]
	v_pk_fma_f32 v[170:171], v[106:107], v[228:229], v[170:171] neg_lo:[0,0,1] neg_hi:[0,0,1]
	v_pk_fma_f32 v[172:173], v[104:105], v[226:227], v[172:173] neg_lo:[0,0,1] neg_hi:[0,0,1]
	v_pk_fma_f32 v[224:225], v[102:103], v[228:229], v[224:225]
	v_lshl_add_u64 v[226:227], v[178:179], 0, v[2:3]
	v_cvt_pk_bf16_f32 v228, v172, v173
	v_cvt_pk_bf16_f32 v229, v170, v171
	v_cvt_pk_bf16_f32 v222, v222, v223
	v_cvt_pk_bf16_f32 v223, v224, v225
	v_and_b32_e32 v15, 0x7cf, v24
	global_store_dwordx2 v[226:227], v[228:229], off
	global_store_dwordx2 v[226:227], v[222:223], off offset:128
	v_lshlrev_b32_e32 v4, 8, v15
	v_mov_b32_e32 v5, v3
	v_lshl_add_u64 v[6:7], v[166:167], 0, v[4:5]
	v_lshl_add_u64 v[4:5], v[168:169], 0, v[4:5]
	s_nop 0
	v_lshlrev_b32_e32 v15, 7, v15
	s_mov_b64 s[26:27], -1
	s_and_b64 vcc, exec, s[4:5]
	v_ashrrev_i32_e32 v35, 31, v34
	v_lshlrev_b32_e32 v170, 1, v15
	s_cbranch_vccnz .LBB0_2003
	s_add_u32 s26, s45, s19
	s_addc_u32 s27, s46, s17
	v_lshlrev_b64 v[172:173], 19, v[34:35]
	v_lshl_add_u64 v[172:173], s[26:27], 0, v[172:173]
	v_mov_b32_e32 v171, v3
	v_lshl_add_u64 v[178:179], v[172:173], 0, v[170:171]
	s_mov_b64 s[26:27], 0

; __device__ __forceinline__ unsigned cvtpk(float lo, float hi) { unsigned r; asm volatile("v_cvt_pk_bf16_f32 %0, %1, %2" : "=v"(r) : "v"(lo), "v"(hi)); return r; }
;     __device__ __forceinline__ void operator()(const f32x4 (&acc)[2][2][4][2], const Unit& u, int wr, int wc, int fr, int fq) const {
;     ...
;                     const float rsc = scale * rr8[ai][m];
;                     const f32x4 c = *(const f32x4*)(cosN + s * 64 + 4 * uu) * rsc, sn = *(const f32x4*)(sinN + s * 64 + 4 * uu) * rsc;
; #pragma unroll
;                     for (int bj = 0; bj < 2; ++bj) { const f32x4 x1 = acc[ai][bj][m][0], x2 = acc[ai][bj][m][1];
;                         const f32x4 o1 = x1 * c - x2 * sn, o2 = x1 * sn + x2 * c;
;                         bf16_t* dst = isq ? (QN + (size_t)t * 1024 + (2 * pn + bj) * 128 + 4 * uu) : (KV6 + (size_t)(pn - 4) * kvstride + ((size_t)(b * 2 + bj) * 2048 + s) * 128 + 4 * uu);
;                         u32x2 w1, w2; w1.x = cvtpk(o1[0], o1[1]); w1.y = cvtpk(o1[2], o1[3]); w2.x = cvtpk(o2[0], o2[1]); w2.y = cvtpk(o2[2], o2[3]);
;                         *(u32x2*)dst = w1; *(u32x2*)(dst + 64) = w2; } }
.LBB0_2005:
	v_mul_f32_e32 v172, v13, v20
	s_waitcnt vmcnt(22)
	v_pk_mul_f32 v[230:231], v[172:173], v[230:231] op_sel_hi:[0,1]
	v_pk_mul_f32 v[234:235], v[172:173], v[234:235] op_sel_hi:[0,1]
	v_pk_mul_f32 v[232:233], v[172:173], v[232:233] op_sel_hi:[0,1]
	v_pk_mul_f32 v[174:175], v[92:93], v[230:231]
	v_pk_mul_f32 v[236:237], v[172:173], v[236:237] op_sel_hi:[0,1]
	v_pk_mul_f32 v[172:173], v[94:95], v[232:233]
	v_pk_fma_f32 v[174:175], v[96:97], v[234:235], v[174:175] neg_lo:[0,0,1] neg_hi:[0,0,1]
	v_pk_fma_f32 v[172:173], v[98:99], v[236:237], v[172:173] neg_lo:[0,0,1] neg_hi:[0,0,1]
	v_pk_mul_f32 v[186:187], v[98:99], v[232:233]
	v_pk_mul_f32 v[196:197], v[96:97], v[230:231]
	v_lshl_add_u64 v[178:179], v[178:179], 0, v[2:3]
	v_cvt_pk_bf16_f32 v174, v174, v175
	v_cvt_pk_bf16_f32 v175, v172, v173
	s_mov_b64 s[26:27], -1
	s_and_b64 vcc, exec, s[4:5]
	v_ashrrev_i32_e32 v33, 31, v32
	v_pk_fma_f32 v[186:187], v[94:95], v[236:237], v[186:187]
	v_pk_fma_f32 v[196:197], v[92:93], v[234:235], v[196:197]
	s_nop 0
	v_cvt_pk_bf16_f32 v172, v196, v197
	v_cvt_pk_bf16_f32 v173, v186, v187
	global_store_dwordx2 v[178:179], v[174:175], off
	global_store_dwordx2 v[178:179], v[172:173], off offset:128
	s_cbranch_vccnz .LBB0_2007
	s_add_u32 s26, s45, s19
	s_addc_u32 s27, s46, s17
	v_lshlrev_b64 v[172:173], 19, v[32:33]
	v_lshl_add_u64 v[172:173], s[26:27], 0, v[172:173]
	v_mov_b32_e32 v171, v3
	v_lshl_add_u64 v[178:179], v[172:173], 0, v[170:171]
	s_mov_b64 s[26:27], 0

; __device__ __forceinline__ unsigned cvtpk(float lo, float hi) { unsigned r; asm volatile("v_cvt_pk_bf16_f32 %0, %1, %2" : "=v"(r) : "v"(lo), "v"(hi)); return r; }
;     __device__ __forceinline__ void operator()(const f32x4 (&acc)[2][2][4][2], const Unit& u, int wr, int wc, int fr, int fq) const {
;     ...
;                     const f32x4 c = *(const f32x4*)(cosN + s * 64 + 4 * uu) * rsc, sn = *(const f32x4*)(sinN + s * 64 + 4 * uu) * rsc;
; #pragma unroll
;                     for (int bj = 0; bj < 2; ++bj) { const f32x4 x1 = acc[ai][bj][m][0], x2 = acc[ai][bj][m][1];
;                         const f32x4 o1 = x1 * c - x2 * sn, o2 = x1 * sn + x2 * c;
;                         bf16_t* dst = isq ? (QN + (size_t)t * 1024 + (2 * pn + bj) * 128 + 4 * uu) : (KV6 + (size_t)(pn - 4) * kvstride + ((size_t)(b * 2 + bj) * 2048 + s) * 128 + 4 * uu);
;                         u32x2 w1, w2; w1.x = cvtpk(o1[0], o1[1]); w1.y = cvtpk(o1[2], o1[3]); w2.x = cvtpk(o2[0], o2[1]); w2.y = cvtpk(o2[2], o2[3]);
;                         *(u32x2*)dst = w1; *(u32x2*)(dst + 64) = w2; } }
.LBB0_2009:
	v_pk_mul_f32 v[172:173], v[80:81], v[230:231]
	v_pk_mul_f32 v[230:231], v[88:89], v[230:231]
	v_pk_mul_f32 v[170:171], v[82:83], v[232:233]
	v_pk_mul_f32 v[232:233], v[90:91], v[232:233]
	v_pk_fma_f32 v[230:231], v[80:81], v[234:235], v[230:231]
	v_add_u32_e32 v176, 0x90, v12
	v_pk_fma_f32 v[170:171], v[90:91], v[236:237], v[170:171] neg_lo:[0,0,1] neg_hi:[0,0,1]
	v_pk_fma_f32 v[172:173], v[88:89], v[234:235], v[172:173] neg_lo:[0,0,1] neg_hi:[0,0,1]
	v_pk_fma_f32 v[232:233], v[82:83], v[236:237], v[232:233]
	v_lshl_add_u64 v[234:235], v[178:179], 0, v[2:3]
	v_cvt_pk_bf16_f32 v236, v172, v173
	v_cvt_pk_bf16_f32 v237, v170, v171
	v_cvt_pk_bf16_f32 v230, v230, v231
	v_cvt_pk_bf16_f32 v231, v232, v233
	v_and_b32_e32 v15, 0x7df, v176
	global_store_dwordx2 v[234:235], v[236:237], off
	global_store_dwordx2 v[234:235], v[230:231], off offset:128
	v_lshlrev_b32_e32 v4, 8, v15
	v_mov_b32_e32 v5, v3
	v_lshl_add_u64 v[6:7], v[166:167], 0, v[4:5]
	v_lshl_add_u64 v[4:5], v[168:169], 0, v[4:5]
	s_nop 0
	v_lshlrev_b32_e32 v15, 7, v15
	s_mov_b64 s[26:27], -1
	s_and_b64 vcc, exec, s[4:5]
	v_lshlrev_b32_e32 v170, 1, v15
	s_cbranch_vccnz .LBB0_2011
	s_add_u32 s26, s45, s19
	s_addc_u32 s27, s46, s17
	v_lshlrev_b64 v[172:173], 19, v[34:35]
	v_lshl_add_u64 v[172:173], s[26:27], 0, v[172:173]
	v_mov_b32_e32 v171, v3
	v_lshl_add_u64 v[178:179], v[172:173], 0, v[170:171]
	s_mov_b64 s[26:27], 0

; __device__ __forceinline__ unsigned cvtpk(float lo, float hi) { unsigned r; asm volatile("v_cvt_pk_bf16_f32 %0, %1, %2" : "=v"(r) : "v"(lo), "v"(hi)); return r; }
;     __device__ __forceinline__ void operator()(const f32x4 (&acc)[2][2][4][2], const Unit& u, int wr, int wc, int fr, int fq) const {
;     ...
;                     const float rsc = scale * rr8[ai][m];
;                     const f32x4 c = *(const f32x4*)(cosN + s * 64 + 4 * uu) * rsc, sn = *(const f32x4*)(sinN + s * 64 + 4 * uu) * rsc;
; #pragma unroll
;                     for (int bj = 0; bj < 2; ++bj) { const f32x4 x1 = acc[ai][bj][m][0], x2 = acc[ai][bj][m][1];
;                         const f32x4 o1 = x1 * c - x2 * sn, o2 = x1 * sn + x2 * c;
;                         bf16_t* dst = isq ? (QN + (size_t)t * 1024 + (2 * pn + bj) * 128 + 4 * uu) : (KV6 + (size_t)(pn - 4) * kvstride + ((size_t)(b * 2 + bj) * 2048 + s) * 128 + 4 * uu);
;                         u32x2 w1, w2; w1.x = cvtpk(o1[0], o1[1]); w1.y = cvtpk(o1[2], o1[3]); w2.x = cvtpk(o2[0], o2[1]); w2.y = cvtpk(o2[2], o2[3]);
;                         *(u32x2*)dst = w1; *(u32x2*)(dst + 64) = w2; } }
.LBB0_2013:
	v_mul_f32_e32 v172, v13, v18
	s_waitcnt vmcnt(24)
	v_pk_mul_f32 v[238:239], v[172:173], v[238:239] op_sel_hi:[0,1]
	v_pk_mul_f32 v[242:243], v[172:173], v[242:243] op_sel_hi:[0,1]
	v_pk_mul_f32 v[240:241], v[172:173], v[240:241] op_sel_hi:[0,1]
	v_pk_mul_f32 v[174:175], v[76:77], v[238:239]
	v_pk_mul_f32 v[244:245], v[172:173], v[244:245] op_sel_hi:[0,1]
	v_pk_mul_f32 v[172:173], v[78:79], v[240:241]
	v_pk_fma_f32 v[174:175], v[84:85], v[242:243], v[174:175] neg_lo:[0,0,1] neg_hi:[0,0,1]
	v_pk_fma_f32 v[172:173], v[86:87], v[244:245], v[172:173] neg_lo:[0,0,1] neg_hi:[0,0,1]
	v_pk_mul_f32 v[186:187], v[86:87], v[240:241]
	v_pk_mul_f32 v[196:197], v[84:85], v[238:239]
	v_lshl_add_u64 v[178:179], v[178:179], 0, v[2:3]
	v_cvt_pk_bf16_f32 v174, v174, v175
	v_cvt_pk_bf16_f32 v175, v172, v173
	s_and_b64 vcc, exec, s[4:5]
	s_mov_b64 s[26:27], -1
	v_pk_fma_f32 v[186:187], v[78:79], v[244:245], v[186:187]
	v_pk_fma_f32 v[196:197], v[76:77], v[242:243], v[196:197]
	s_nop 0
	v_cvt_pk_bf16_f32 v172, v196, v197
	v_cvt_pk_bf16_f32 v173, v186, v187
	global_store_dwordx2 v[178:179], v[174:175], off
	global_store_dwordx2 v[178:179], v[172:173], off offset:128
	s_cbranch_vccnz .LBB0_2015
	s_add_u32 s26, s45, s19
	s_addc_u32 s27, s46, s17
	v_lshlrev_b64 v[172:173], 19, v[32:33]
	v_lshl_add_u64 v[172:173], s[26:27], 0, v[172:173]
	v_mov_b32_e32 v171, v3
	v_lshl_add_u64 v[178:179], v[172:173], 0, v[170:171]
	s_mov_b64 s[26:27], 0

; __device__ __forceinline__ unsigned cvtpk(float lo, float hi) { unsigned r; asm volatile("v_cvt_pk_bf16_f32 %0, %1, %2" : "=v"(r) : "v"(lo), "v"(hi)); return r; }
;     __device__ __forceinline__ void operator()(const f32x4 (&acc)[2][2][4][2], const Unit& u, int wr, int wc, int fr, int fq) const {
;     ...
;                     const f32x4 c = *(const f32x4*)(cosN + s * 64 + 4 * uu) * rsc, sn = *(const f32x4*)(sinN + s * 64 + 4 * uu) * rsc;
; #pragma unroll
;                     for (int bj = 0; bj < 2; ++bj) { const f32x4 x1 = acc[ai][bj][m][0], x2 = acc[ai][bj][m][1];
;                         const f32x4 o1 = x1 * c - x2 * sn, o2 = x1 * sn + x2 * c;
;                         bf16_t* dst = isq ? (QN + (size_t)t * 1024 + (2 * pn + bj) * 128 + 4 * uu) : (KV6 + (size_t)(pn - 4) * kvstride + ((size_t)(b * 2 + bj) * 2048 + s) * 128 + 4 * uu);
;                         u32x2 w1, w2; w1.x = cvtpk(o1[0], o1[1]); w1.y = cvtpk(o1[2], o1[3]); w2.x = cvtpk(o2[0], o2[1]); w2.y = cvtpk(o2[2], o2[3]);
;                         *(u32x2*)dst = w1; *(u32x2*)(dst + 64) = w2; } }
.LBB0_2017:
	v_pk_mul_f32 v[172:173], v[64:65], v[238:239]
	v_pk_mul_f32 v[238:239], v[72:73], v[238:239]
	v_pk_mul_f32 v[170:171], v[66:67], v[240:241]
	v_pk_mul_f32 v[240:241], v[74:75], v[240:241]
	v_pk_fma_f32 v[238:239], v[64:65], v[242:243], v[238:239]
	v_add_u32_e32 v176, 0xa0, v12
	v_pk_fma_f32 v[170:171], v[74:75], v[244:245], v[170:171] neg_lo:[0,0,1] neg_hi:[0,0,1]
	v_pk_fma_f32 v[172:173], v[72:73], v[242:243], v[172:173] neg_lo:[0,0,1] neg_hi:[0,0,1]
	v_pk_fma_f32 v[240:241], v[66:67], v[244:245], v[240:241]
	v_lshl_add_u64 v[242:243], v[178:179], 0, v[2:3]
	v_cvt_pk_bf16_f32 v244, v172, v173
	v_cvt_pk_bf16_f32 v245, v170, v171
	v_cvt_pk_bf16_f32 v238, v238, v239
	v_cvt_pk_bf16_f32 v239, v240, v241
	v_and_b32_e32 v15, 0x7ef, v176
	global_store_dwordx2 v[242:243], v[244:245], off
	global_store_dwordx2 v[242:243], v[238:239], off offset:128
	v_lshlrev_b32_e32 v4, 8, v15
	v_mov_b32_e32 v5, v3
	v_lshl_add_u64 v[6:7], v[166:167], 0, v[4:5]
	v_lshl_add_u64 v[4:5], v[168:169], 0, v[4:5]
	s_nop 0
	v_lshlrev_b32_e32 v15, 7, v15
	s_mov_b64 s[26:27], -1
	s_and_b64 vcc, exec, s[4:5]
	v_lshlrev_b32_e32 v170, 1, v15
	s_cbranch_vccnz .LBB0_2019
	s_add_u32 s26, s45, s19
	s_addc_u32 s27, s46, s17
	v_lshlrev_b64 v[172:173], 19, v[34:35]
	v_lshl_add_u64 v[172:173], s[26:27], 0, v[172:173]
	v_mov_b32_e32 v171, v3
	v_lshl_add_u64 v[178:179], v[172:173], 0, v[170:171]
	s_mov_b64 s[26:27], 0

; __device__ __forceinline__ unsigned cvtpk(float lo, float hi) { unsigned r; asm volatile("v_cvt_pk_bf16_f32 %0, %1, %2" : "=v"(r) : "v"(lo), "v"(hi)); return r; }
;     __device__ __forceinline__ void operator()(const f32x4 (&acc)[2][2][4][2], const Unit& u, int wr, int wc, int fr, int fq) const {
;     ...
;                     const float rsc = scale * rr8[ai][m];
;                     const f32x4 c = *(const f32x4*)(cosN + s * 64 + 4 * uu) * rsc, sn = *(const f32x4*)(sinN + s * 64 + 4 * uu) * rsc;
; #pragma unroll
;                     for (int bj = 0; bj < 2; ++bj) { const f32x4 x1 = acc[ai][bj][m][0], x2 = acc[ai][bj][m][1];
;                         const f32x4 o1 = x1 * c - x2 * sn, o2 = x1 * sn + x2 * c;
;                         bf16_t* dst = isq ? (QN + (size_t)t * 1024 + (2 * pn + bj) * 128 + 4 * uu) : (KV6 + (size_t)(pn - 4) * kvstride + ((size_t)(b * 2 + bj) * 2048 + s) * 128 + 4 * uu);
;                         u32x2 w1, w2; w1.x = cvtpk(o1[0], o1[1]); w1.y = cvtpk(o1[2], o1[3]); w2.x = cvtpk(o2[0], o2[1]); w2.y = cvtpk(o2[2], o2[3]);
;                         *(u32x2*)dst = w1; *(u32x2*)(dst + 64) = w2; } }
.LBB0_2021:
	v_mul_f32_e32 v172, v13, v16
	s_waitcnt vmcnt(18)
	v_pk_mul_f32 v[206:207], v[172:173], v[206:207] op_sel_hi:[0,1]
	v_pk_mul_f32 v[210:211], v[172:173], v[210:211] op_sel_hi:[0,1]
	v_pk_mul_f32 v[208:209], v[172:173], v[208:209] op_sel_hi:[0,1]
	v_pk_mul_f32 v[174:175], v[60:61], v[206:207]
	v_pk_mul_f32 v[212:213], v[172:173], v[212:213] op_sel_hi:[0,1]
	v_pk_mul_f32 v[172:173], v[62:63], v[208:209]
	v_pk_fma_f32 v[174:175], v[68:69], v[210:211], v[174:175] neg_lo:[0,0,1] neg_hi:[0,0,1]
	v_pk_fma_f32 v[172:173], v[70:71], v[212:213], v[172:173] neg_lo:[0,0,1] neg_hi:[0,0,1]
	v_pk_mul_f32 v[186:187], v[70:71], v[208:209]
	v_pk_mul_f32 v[196:197], v[68:69], v[206:207]
	v_lshl_add_u64 v[178:179], v[178:179], 0, v[2:3]
	v_cvt_pk_bf16_f32 v174, v174, v175
	v_cvt_pk_bf16_f32 v175, v172, v173
	s_and_b64 vcc, exec, s[4:5]
	s_mov_b64 s[26:27], -1
	v_pk_fma_f32 v[186:187], v[62:63], v[212:213], v[186:187]
	v_pk_fma_f32 v[196:197], v[60:61], v[210:211], v[196:197]
	s_nop 0
	v_cvt_pk_bf16_f32 v172, v196, v197
	v_cvt_pk_bf16_f32 v173, v186, v187
	global_store_dwordx2 v[178:179], v[174:175], off
	global_store_dwordx2 v[178:179], v[172:173], off offset:128
	s_cbranch_vccnz .LBB0_2023
	s_add_u32 s26, s45, s19
	s_addc_u32 s27, s46, s17
	v_lshlrev_b64 v[172:173], 19, v[32:33]
	v_lshl_add_u64 v[172:173], s[26:27], 0, v[172:173]
	v_mov_b32_e32 v171, v3
	v_lshl_add_u64 v[178:179], v[172:173], 0, v[170:171]
	s_mov_b64 s[26:27], 0

; __device__ __forceinline__ unsigned cvtpk(float lo, float hi) { unsigned r; asm volatile("v_cvt_pk_bf16_f32 %0, %1, %2" : "=v"(r) : "v"(lo), "v"(hi)); return r; }
;     __device__ __forceinline__ void operator()(const f32x4 (&acc)[2][2][4][2], const Unit& u, int wr, int wc, int fr, int fq) const {
;     ...
;                     const f32x4 c = *(const f32x4*)(cosN + s * 64 + 4 * uu) * rsc, sn = *(const f32x4*)(sinN + s * 64 + 4 * uu) * rsc;
; #pragma unroll
;                     for (int bj = 0; bj < 2; ++bj) { const f32x4 x1 = acc[ai][bj][m][0], x2 = acc[ai][bj][m][1];
;                         const f32x4 o1 = x1 * c - x2 * sn, o2 = x1 * sn + x2 * c;
;                         bf16_t* dst = isq ? (QN + (size_t)t * 1024 + (2 * pn + bj) * 128 + 4 * uu) : (KV6 + (size_t)(pn - 4) * kvstride + ((size_t)(b * 2 + bj) * 2048 + s) * 128 + 4 * uu);
;                         u32x2 w1, w2; w1.x = cvtpk(o1[0], o1[1]); w1.y = cvtpk(o1[2], o1[3]); w2.x = cvtpk(o2[0], o2[1]); w2.y = cvtpk(o2[2], o2[3]);
;                         *(u32x2*)dst = w1; *(u32x2*)(dst + 64) = w2; } }
.LBB0_2025:
	v_pk_mul_f32 v[172:173], v[48:49], v[206:207]
	v_pk_mul_f32 v[206:207], v[56:57], v[206:207]
	v_pk_mul_f32 v[170:171], v[50:51], v[208:209]
	v_pk_fma_f32 v[172:173], v[56:57], v[210:211], v[172:173] neg_lo:[0,0,1] neg_hi:[0,0,1]
	v_pk_mul_f32 v[208:209], v[58:59], v[208:209]
	v_pk_fma_f32 v[206:207], v[48:49], v[210:211], v[206:207]
	v_lshl_add_u64 v[210:211], v[178:179], 0, v[2:3]
	v_add_u32_e32 v178, 0xb0, v12
	v_pk_fma_f32 v[170:171], v[58:59], v[212:213], v[170:171] neg_lo:[0,0,1] neg_hi:[0,0,1]
	v_pk_fma_f32 v[208:209], v[50:51], v[212:213], v[208:209]
	v_cvt_pk_bf16_f32 v212, v172, v173
	v_cvt_pk_bf16_f32 v213, v170, v171
	v_cvt_pk_bf16_f32 v206, v206, v207
	v_and_b32_e32 v15, 0x7ff, v178
	v_cvt_pk_bf16_f32 v207, v208, v209
	global_store_dwordx2 v[210:211], v[212:213], off
	global_store_dwordx2 v[210:211], v[206:207], off offset:128
	v_lshlrev_b32_e32 v4, 8, v15
	v_mov_b32_e32 v5, v3
	v_lshl_add_u64 v[6:7], v[166:167], 0, v[4:5]
	v_lshl_add_u64 v[4:5], v[168:169], 0, v[4:5]
	s_nop 0
	v_lshlrev_b32_e32 v15, 7, v15
	s_mov_b64 s[26:27], -1
	s_and_b64 vcc, exec, s[4:5]
	v_lshlrev_b32_e32 v170, 1, v15
	s_cbranch_vccnz .LBB0_2027
	s_add_u32 s26, s45, s19
	s_addc_u32 s27, s46, s17
	v_lshlrev_b64 v[34:35], 19, v[34:35]
	v_lshl_add_u64 v[34:35], s[26:27], 0, v[34:35]
	v_mov_b32_e32 v171, v3
	v_lshl_add_u64 v[176:177], v[34:35], 0, v[170:171]
	s_mov_b64 s[26:27], 0

; __device__ __forceinline__ unsigned cvtpk(float lo, float hi) { unsigned r; asm volatile("v_cvt_pk_bf16_f32 %0, %1, %2" : "=v"(r) : "v"(lo), "v"(hi)); return r; }
;     __device__ __forceinline__ void operator()(const f32x4 (&acc)[2][2][4][2], const Unit& u, int wr, int wc, int fr, int fq) const {
;     ...
;                     const float rsc = scale * rr8[ai][m];
;                     const f32x4 c = *(const f32x4*)(cosN + s * 64 + 4 * uu) * rsc, sn = *(const f32x4*)(sinN + s * 64 + 4 * uu) * rsc;
; #pragma unroll
;                     for (int bj = 0; bj < 2; ++bj) { const f32x4 x1 = acc[ai][bj][m][0], x2 = acc[ai][bj][m][1];
;                         const f32x4 o1 = x1 * c - x2 * sn, o2 = x1 * sn + x2 * c;
;                         bf16_t* dst = isq ? (QN + (size_t)t * 1024 + (2 * pn + bj) * 128 + 4 * uu) : (KV6 + (size_t)(pn - 4) * kvstride + ((size_t)(b * 2 + bj) * 2048 + s) * 128 + 4 * uu);
;                         u32x2 w1, w2; w1.x = cvtpk(o1[0], o1[1]); w1.y = cvtpk(o1[2], o1[3]); w2.x = cvtpk(o2[0], o2[1]); w2.y = cvtpk(o2[2], o2[3]);
;                         *(u32x2*)dst = w1; *(u32x2*)(dst + 64) = w2; } }
.LBB0_2029:
	v_mul_f32_e32 v172, v13, v14
	s_waitcnt vmcnt(16)
	v_pk_mul_f32 v[214:215], v[172:173], v[214:215] op_sel_hi:[0,1]
	v_pk_mul_f32 v[218:219], v[172:173], v[218:219] op_sel_hi:[0,1]
	v_pk_mul_f32 v[216:217], v[172:173], v[216:217] op_sel_hi:[0,1]
	v_pk_mul_f32 v[174:175], v[44:45], v[214:215]
	v_pk_mul_f32 v[220:221], v[172:173], v[220:221] op_sel_hi:[0,1]
	v_pk_mul_f32 v[172:173], v[46:47], v[216:217]
	v_pk_fma_f32 v[174:175], v[52:53], v[218:219], v[174:175] neg_lo:[0,0,1] neg_hi:[0,0,1]
	v_pk_fma_f32 v[172:173], v[54:55], v[220:221], v[172:173] neg_lo:[0,0,1] neg_hi:[0,0,1]
	v_pk_mul_f32 v[178:179], v[54:55], v[216:217]
	v_pk_mul_f32 v[186:187], v[52:53], v[214:215]
	v_lshl_add_u64 v[176:177], v[176:177], 0, v[2:3]
	v_cvt_pk_bf16_f32 v174, v174, v175
	v_cvt_pk_bf16_f32 v175, v172, v173
	s_and_b64 vcc, exec, s[4:5]
	s_mov_b64 s[4:5], -1
	v_pk_fma_f32 v[178:179], v[46:47], v[220:221], v[178:179]
	v_pk_fma_f32 v[186:187], v[44:45], v[218:219], v[186:187]
	s_nop 0
	v_cvt_pk_bf16_f32 v172, v186, v187
	v_cvt_pk_bf16_f32 v173, v178, v179
	global_store_dwordx2 v[176:177], v[174:175], off
	global_store_dwordx2 v[176:177], v[172:173], off offset:128
	s_cbranch_vccnz .LBB0_2031
	s_add_u32 s4, s45, s19
	s_addc_u32 s5, s46, s17
	v_lshlrev_b64 v[32:33], 19, v[32:33]
	v_lshl_add_u64 v[32:33], s[4:5], 0, v[32:33]
	v_mov_b32_e32 v171, v3
	v_lshl_add_u64 v[176:177], v[32:33], 0, v[170:171]
	s_mov_b64 s[4:5], 0

; __device__ __forceinline__ unsigned cvtpk(float lo, float hi) { unsigned r; asm volatile("v_cvt_pk_bf16_f32 %0, %1, %2" : "=v"(r) : "v"(lo), "v"(hi)); return r; }
;     __device__ __forceinline__ void operator()(const f32x4 (&acc)[2][2][4][2], const Unit& u, int wr, int wc, int fr, int fq) const {
;     ...
;                     const f32x4 c = *(const f32x4*)(cosN + s * 64 + 4 * uu) * rsc, sn = *(const f32x4*)(sinN + s * 64 + 4 * uu) * rsc;
; #pragma unroll
;                     for (int bj = 0; bj < 2; ++bj) { const f32x4 x1 = acc[ai][bj][m][0], x2 = acc[ai][bj][m][1];
;                         const f32x4 o1 = x1 * c - x2 * sn, o2 = x1 * sn + x2 * c;
;                         bf16_t* dst = isq ? (QN + (size_t)t * 1024 + (2 * pn + bj) * 128 + 4 * uu) : (KV6 + (size_t)(pn - 4) * kvstride + ((size_t)(b * 2 + bj) * 2048 + s) * 128 + 4 * uu);
;                         u32x2 w1, w2; w1.x = cvtpk(o1[0], o1[1]); w1.y = cvtpk(o1[2], o1[3]); w2.x = cvtpk(o2[0], o2[1]); w2.y = cvtpk(o2[2], o2[3]);
;                         *(u32x2*)dst = w1; *(u32x2*)(dst + 64) = w2; } }
.LBB0_2033:
	v_pk_mul_f32 v[32:33], v[38:39], v[216:217]
	v_pk_mul_f32 v[34:35], v[36:37], v[214:215]
	v_pk_mul_f32 v[216:217], v[42:43], v[216:217]
	v_pk_mul_f32 v[214:215], v[40:41], v[214:215]
	v_pk_fma_f32 v[32:33], v[42:43], v[220:221], v[32:33] neg_lo:[0,0,1] neg_hi:[0,0,1]
	v_pk_fma_f32 v[34:35], v[40:41], v[218:219], v[34:35] neg_lo:[0,0,1] neg_hi:[0,0,1]
	v_pk_fma_f32 v[216:217], v[38:39], v[220:221], v[216:217]
	v_pk_fma_f32 v[214:215], v[36:37], v[218:219], v[214:215]
	v_lshl_add_u64 v[218:219], v[176:177], 0, v[2:3]
	v_cvt_pk_bf16_f32 v220, v34, v35
	v_cvt_pk_bf16_f32 v221, v32, v33
	v_cvt_pk_bf16_f32 v214, v214, v215
	v_cvt_pk_bf16_f32 v215, v216, v217
	global_store_dwordx2 v[218:219], v[220:221], off
	global_store_dwordx2 v[218:219], v[214:215], off offset:128

; __device__ __forceinline__ float bflo(unsigned x) { return __uint_as_float(x << 16); }
; __device__ __forceinline__ float bfhi(unsigned x) { return __uint_as_float(x & 0xffff0000u); }
; __device__ __forceinline__ unsigned cvtpk(float lo, float hi) { unsigned r; asm volatile("v_cvt_pk_bf16_f32 %0, %1, %2" : "=v"(r) : "v"(lo), "v"(hi)); return r; }
;     ...
;             asm volatile("s_nop 7\n\ts_nop 7\n\ts_nop 3" ::: "memory");
;     __device__ __forceinline__ void operator()(const f32x4 (&acc)[2][2][4][2], const Unit& u, int wr, int wc, int fr, int fq) const {
;     ...
;         if constexpr (PLAIN) {
; #pragma unroll
;             for (int ai = 0; ai < 2; ++ai)
; #pragma unroll
;                 for (int m = 0; m < 4; ++m) { const size_t off = (size_t)(row0 + ai * HALF + m * 16) * ldc + col0;
;                     const u32x4 ra = *(const u32x4*)((const bf16_t*)res + off), rb = *(const u32x4*)((const bf16_t*)res + off + HALF);
; #pragma unroll
;                     for (int bj = 0; bj < 2; ++bj) { const u32x4 w_ = bj ? rb : ra; const f32x4 v0 = (f32x4){bflo(w_.x), bfhi(w_.x), bflo(w_.y), bfhi(w_.y)} + acc[ai][bj][m][0], v1 = (f32x4){bflo(w_.z), bfhi(w_.z), bflo(w_.w), bfhi(w_.w)} + acc[ai][bj][m][1];
;                         u32x4 w; w.x = cvtpk(v0[0], v0[1]); w.y = cvtpk(v0[2], v0[3]); w.z = cvtpk(v1[0], v1[1]); w.w = cvtpk(v1[2], v1[3]);
;                         *(u32x4*)(out + off + bj * HALF) = w; }
;                     asm volatile("" ::: "memory"); }
.LBB0_2589:
	v_lshl_add_u32 v6, s51, 8, v167
	v_lshl_or_b32 v4, s50, 8, v168
	v_ashrrev_i32_e32 v7, 31, v6
	v_readlane_b32 s52, v250, 34
	v_ashrrev_i32_e32 v5, 31, v4
	v_lshlrev_b64 v[0:1], 11, v[6:7]
	v_readlane_b32 s53, v250, 35
	v_readlane_b32 s54, v250, 36
	v_readlane_b32 s55, v250, 37
	v_readlane_b32 s56, v250, 38
	v_readlane_b32 s57, v250, 39
	v_readlane_b32 s58, v250, 40
	v_readlane_b32 s59, v250, 41
	v_readlane_b32 s60, v250, 42
	v_readlane_b32 s61, v250, 43
	v_readlane_b32 s62, v250, 44
	v_readlane_b32 s63, v250, 45
	v_lshl_add_u64 v[0:1], v[0:1], 0, v[4:5]
	v_readlane_b32 s64, v250, 46
	v_readlane_b32 s65, v250, 47
	v_readlane_b32 s66, v250, 48
	v_readlane_b32 s67, v250, 49
	s_mov_b64 s[52:53], s[56:57]
	v_lshlrev_b64 v[0:1], 1, v[0:1]
	s_mov_b64 s[54:55], s[58:59]
	s_mov_b64 s[56:57], s[60:61]
	s_mov_b64 s[58:59], s[62:63]
	s_mov_b64 s[60:61], s[64:65]
	s_mov_b64 s[62:63], s[66:67]
	v_lshl_add_u64 v[12:13], s[62:63], 0, v[0:1]
	s_nop 7
	s_nop 7
	s_nop 3
	s_mov_b64 s[100:101], 0x10000
	v_lshl_add_u64 v[248:249], s[100:101], 0, v[12:13]
	global_load_dwordx4 v[208:211], v[248:249], off
	global_load_dwordx4 v[212:215], v[248:249], off offset:256
	s_mov_b64 s[100:101], 0x20000
	v_lshl_add_u64 v[248:249], s[100:101], 0, v[12:13]
	global_load_dwordx4 v[216:219], v[248:249], off
	global_load_dwordx4 v[220:223], v[248:249], off offset:256
	s_mov_b64 s[100:101], 0x30000
	v_lshl_add_u64 v[248:249], s[100:101], 0, v[12:13]
	global_load_dwordx4 v[224:227], v[248:249], off
	global_load_dwordx4 v[228:231], v[248:249], off offset:256
	s_mov_b64 s[100:101], 0x80000
	v_lshl_add_u64 v[248:249], s[100:101], 0, v[12:13]
	global_load_dwordx4 v[232:235], v[248:249], off
	global_load_dwordx4 v[236:239], v[248:249], off offset:256
	s_mov_b64 s[100:101], 0x90000
	v_lshl_add_u64 v[248:249], s[100:101], 0, v[12:13]
	global_load_dwordx4 v[240:243], v[248:249], off
	global_load_dwordx4 v[244:247], v[248:249], off offset:256
	s_mov_b64 s[100:101], 0xa0000
	v_lshl_add_u64 v[248:249], s[100:101], 0, v[12:13]
	global_load_dwordx4 v[24:27], v[248:249], off
	global_load_dwordx4 v[28:31], v[248:249], off offset:256
	s_mov_b64 s[100:101], 0xb0000
	v_lshl_add_u64 v[248:249], s[100:101], 0, v[12:13]
	global_load_dwordx4 v[196:199], v[248:249], off
	global_load_dwordx4 v[180:183], v[248:249], off offset:256
	global_load_dwordx4 v[8:11], v[12:13], off
	s_nop 0
	global_load_dwordx4 v[12:15], v[12:13], off offset:256
	s_mov_b64 s[18:19], 0x80000
	s_andn2_b64 vcc, exec, s[2:3]
	s_waitcnt vmcnt(1)
	v_lshlrev_b32_e32 v16, 16, v8
	v_and_b32_e32 v17, 0xffff0000, v8
	v_lshlrev_b32_e32 v8, 16, v9
	v_and_b32_e32 v9, 0xffff0000, v9
	v_pk_add_f32 v[18:19], v[162:163], v[8:9]
	v_pk_add_f32 v[8:9], v[160:161], v[16:17]
	v_lshlrev_b32_e32 v16, 16, v10
	v_and_b32_e32 v17, 0xffff0000, v10
	v_lshlrev_b32_e32 v10, 16, v11
	v_and_b32_e32 v11, 0xffff0000, v11
	v_pk_add_f32 v[20:21], v[158:159], v[10:11]
	v_pk_add_f32 v[10:11], v[156:157], v[16:17]
	v_cvt_pk_bf16_f32 v8, v8, v9
	v_cvt_pk_bf16_f32 v9, v18, v19
	v_lshl_add_u64 v[16:17], s[6:7], 0, v[0:1]
	v_cvt_pk_bf16_f32 v10, v10, v11
	v_cvt_pk_bf16_f32 v11, v20, v21
	global_store_dwordx4 v[16:17], v[8:11], off
	s_waitcnt vmcnt(1)
	s_nop 0
	v_lshlrev_b32_e32 v8, 16, v12
	v_and_b32_e32 v9, 0xffff0000, v12
	v_lshlrev_b32_e32 v10, 16, v13
	v_and_b32_e32 v11, 0xffff0000, v13
	v_pk_add_f32 v[8:9], v[152:153], v[8:9]
	v_pk_add_f32 v[10:11], v[154:155], v[10:11]
	v_lshlrev_b32_e32 v12, 16, v14
	v_and_b32_e32 v13, 0xffff0000, v14
	v_lshlrev_b32_e32 v14, 16, v15
	v_and_b32_e32 v15, 0xffff0000, v15
	v_cvt_pk_bf16_f32 v8, v8, v9
	v_pk_add_f32 v[14:15], v[150:151], v[14:15]
	v_pk_add_f32 v[12:13], v[148:149], v[12:13]
	v_cvt_pk_bf16_f32 v9, v10, v11
	s_nop 0
	v_cvt_pk_bf16_f32 v10, v12, v13
	v_cvt_pk_bf16_f32 v11, v14, v15
	global_store_dwordx4 v[16:17], v[8:11], off offset:256
	s_nop 1
	v_or_b32_e32 v8, 16, v6
	v_ashrrev_i32_e32 v9, 31, v8
	v_lshlrev_b64 v[8:9], 11, v[8:9]
	v_lshl_add_u64 v[8:9], v[8:9], 0, v[4:5]
	v_lshlrev_b64 v[16:17], 1, v[8:9]
	v_lshl_add_u64 v[12:13], s[62:63], 0, v[16:17]
	s_nop 0
	v_lshl_add_u64 v[16:17], s[6:7], 0, v[16:17]
	s_nop 0
	v_lshlrev_b32_e32 v18, 16, v208
	v_and_b32_e32 v19, 0xffff0000, v208
	v_lshlrev_b32_e32 v208, 16, v209
	v_and_b32_e32 v209, 0xffff0000, v209
	v_pk_add_f32 v[20:21], v[146:147], v[208:209]
	v_pk_add_f32 v[208:209], v[144:145], v[18:19]
	v_lshlrev_b32_e32 v18, 16, v210
	v_and_b32_e32 v19, 0xffff0000, v210
	v_lshlrev_b32_e32 v210, 16, v211
	v_and_b32_e32 v211, 0xffff0000, v211
	v_pk_add_f32 v[22:23], v[142:143], v[210:211]
	v_pk_add_f32 v[210:211], v[140:141], v[18:19]
	v_cvt_pk_bf16_f32 v208, v208, v209
	v_cvt_pk_bf16_f32 v209, v20, v21
	s_nop 0
	v_cvt_pk_bf16_f32 v210, v210, v211
	v_cvt_pk_bf16_f32 v211, v22, v23
	global_store_dwordx4 v[16:17], v[208:211], off
	s_nop 0
	s_nop 0
	v_lshlrev_b32_e32 v208, 16, v212
	v_and_b32_e32 v209, 0xffff0000, v212
	v_lshlrev_b32_e32 v210, 16, v213
	v_and_b32_e32 v211, 0xffff0000, v213
	v_pk_add_f32 v[208:209], v[136:137], v[208:209]
	v_pk_add_f32 v[210:211], v[138:139], v[210:211]
	v_lshlrev_b32_e32 v212, 16, v214
	v_and_b32_e32 v213, 0xffff0000, v214
	v_lshlrev_b32_e32 v214, 16, v215
	v_and_b32_e32 v215, 0xffff0000, v215
	v_cvt_pk_bf16_f32 v208, v208, v209
	v_pk_add_f32 v[214:215], v[134:135], v[214:215]
	v_pk_add_f32 v[212:213], v[132:133], v[212:213]
	v_cvt_pk_bf16_f32 v209, v210, v211
	s_nop 0
	v_cvt_pk_bf16_f32 v210, v212, v213
	v_cvt_pk_bf16_f32 v211, v214, v215
	global_store_dwordx4 v[16:17], v[208:211], off offset:256
	s_nop 1
	v_or_b32_e32 v8, 32, v6
	v_ashrrev_i32_e32 v9, 31, v8
	v_lshlrev_b64 v[8:9], 11, v[8:9]
	v_lshl_add_u64 v[8:9], v[8:9], 0, v[4:5]
; __device__ __forceinline__ float bflo(unsigned x) { return __uint_as_float(x << 16); }
; __device__ __forceinline__ float bfhi(unsigned x) { return __uint_as_float(x & 0xffff0000u); }
; __device__ __forceinline__ unsigned cvtpk(float lo, float hi) { unsigned r; asm volatile("v_cvt_pk_bf16_f32 %0, %1, %2" : "=v"(r) : "v"(lo), "v"(hi)); return r; }
;     __device__ __forceinline__ void operator()(const f32x4 (&acc)[2][2][4][2], const Unit& u, int wr, int wc, int fr, int fq) const {
;     ...
;                 for (int m = 0; m < 4; ++m) { const size_t off = (size_t)(row0 + ai * HALF + m * 16) * ldc + col0;
;                     const u32x4 ra = *(const u32x4*)((const bf16_t*)res + off), rb = *(const u32x4*)((const bf16_t*)res + off + HALF);
; #pragma unroll
;                     for (int bj = 0; bj < 2; ++bj) { const u32x4 w_ = bj ? rb : ra; const f32x4 v0 = (f32x4){bflo(w_.x), bfhi(w_.x), bflo(w_.y), bfhi(w_.y)} + acc[ai][bj][m][0], v1 = (f32x4){bflo(w_.z), bfhi(w_.z), bflo(w_.w), bfhi(w_.w)} + acc[ai][bj][m][1];
;                         u32x4 w; w.x = cvtpk(v0[0], v0[1]); w.y = cvtpk(v0[2], v0[3]); w.z = cvtpk(v1[0], v1[1]); w.w = cvtpk(v1[2], v1[3]);
;                         *(u32x4*)(out + off + bj * HALF) = w; }
;                     asm volatile("" ::: "memory"); }
	v_lshlrev_b64 v[16:17], 1, v[8:9]
	v_lshl_add_u64 v[12:13], s[62:63], 0, v[16:17]
	s_nop 0
	v_or_b32_e32 v6, 48, v6
	v_lshl_add_u64 v[16:17], s[6:7], 0, v[16:17]
	v_ashrrev_i32_e32 v7, 31, v6
	v_lshlrev_b64 v[6:7], 11, v[6:7]
	v_lshl_add_u64 v[4:5], v[6:7], 0, v[4:5]
	s_nop 0
	v_lshlrev_b32_e32 v18, 16, v216
	v_and_b32_e32 v19, 0xffff0000, v216
	v_lshlrev_b32_e32 v216, 16, v217
	v_and_b32_e32 v217, 0xffff0000, v217
	v_pk_add_f32 v[20:21], v[130:131], v[216:217]
	v_pk_add_f32 v[216:217], v[128:129], v[18:19]
	v_lshlrev_b32_e32 v18, 16, v218
	v_and_b32_e32 v19, 0xffff0000, v218
	v_lshlrev_b32_e32 v218, 16, v219
	v_and_b32_e32 v219, 0xffff0000, v219
	v_pk_add_f32 v[22:23], v[126:127], v[218:219]
	v_pk_add_f32 v[218:219], v[124:125], v[18:19]
	v_cvt_pk_bf16_f32 v216, v216, v217
	v_cvt_pk_bf16_f32 v217, v20, v21
	s_nop 0
	v_cvt_pk_bf16_f32 v218, v218, v219
	v_cvt_pk_bf16_f32 v219, v22, v23
	global_store_dwordx4 v[16:17], v[216:219], off
	s_nop 0
	s_nop 0
	v_lshlrev_b32_e32 v216, 16, v220
	v_and_b32_e32 v217, 0xffff0000, v220
	v_lshlrev_b32_e32 v218, 16, v221
	v_and_b32_e32 v219, 0xffff0000, v221
	v_lshlrev_b32_e32 v220, 16, v222
	v_and_b32_e32 v221, 0xffff0000, v222
	v_pk_add_f32 v[218:219], v[122:123], v[218:219]
	v_pk_add_f32 v[216:217], v[120:121], v[216:217]
	v_lshlrev_b32_e32 v222, 16, v223
	v_and_b32_e32 v223, 0xffff0000, v223
	v_pk_add_f32 v[220:221], v[116:117], v[220:221]
	v_pk_add_f32 v[222:223], v[118:119], v[222:223]
	v_cvt_pk_bf16_f32 v216, v216, v217
	v_cvt_pk_bf16_f32 v217, v218, v219
	v_cvt_pk_bf16_f32 v218, v220, v221
	v_lshlrev_b64 v[12:13], 1, v[4:5]
	v_cvt_pk_bf16_f32 v219, v222, v223
	global_store_dwordx4 v[16:17], v[216:219], off offset:256
	s_nop 1
	v_lshl_add_u64 v[8:9], s[62:63], 0, v[12:13]
	s_nop 0
	v_lshl_add_u64 v[12:13], s[6:7], 0, v[12:13]
	s_nop 0
	v_lshlrev_b32_e32 v14, 16, v224
	v_and_b32_e32 v15, 0xffff0000, v224
	v_lshlrev_b32_e32 v224, 16, v225
	v_and_b32_e32 v225, 0xffff0000, v225
	v_pk_add_f32 v[16:17], v[114:115], v[224:225]
	v_pk_add_f32 v[224:225], v[112:113], v[14:15]
	v_lshlrev_b32_e32 v14, 16, v226
	v_and_b32_e32 v15, 0xffff0000, v226
	v_lshlrev_b32_e32 v226, 16, v227
	v_and_b32_e32 v227, 0xffff0000, v227
	v_pk_add_f32 v[18:19], v[110:111], v[226:227]
	v_pk_add_f32 v[226:227], v[108:109], v[14:15]
	v_cvt_pk_bf16_f32 v224, v224, v225
	v_cvt_pk_bf16_f32 v225, v16, v17
	s_nop 0
	v_cvt_pk_bf16_f32 v226, v226, v227
	v_cvt_pk_bf16_f32 v227, v18, v19
	global_store_dwordx4 v[12:13], v[224:227], off
	s_nop 0
	s_nop 0
	v_lshlrev_b32_e32 v224, 16, v228
	v_and_b32_e32 v225, 0xffff0000, v228
	v_lshlrev_b32_e32 v226, 16, v229
	v_and_b32_e32 v227, 0xffff0000, v229
	v_pk_add_f32 v[226:227], v[106:107], v[226:227]
	v_pk_add_f32 v[224:225], v[104:105], v[224:225]
	v_lshlrev_b32_e32 v228, 16, v230
	v_and_b32_e32 v229, 0xffff0000, v230
	v_lshlrev_b32_e32 v230, 16, v231
	v_and_b32_e32 v231, 0xffff0000, v231
	v_pk_add_f32 v[230:231], v[102:103], v[230:231]
	v_pk_add_f32 v[228:229], v[100:101], v[228:229]
	v_cvt_pk_bf16_f32 v224, v224, v225
	v_cvt_pk_bf16_f32 v225, v226, v227
	s_nop 0
	v_cvt_pk_bf16_f32 v226, v228, v229
	v_cvt_pk_bf16_f32 v227, v230, v231
	global_store_dwordx4 v[12:13], v[224:227], off offset:256
	v_lshl_add_u64 v[12:13], v[0:1], 0, s[18:19]
	v_lshl_add_u64 v[8:9], s[62:63], 0, v[12:13]
	s_nop 0
	v_lshl_add_u64 v[12:13], s[6:7], 0, v[12:13]
	s_mov_b64 s[18:19], 0x90000
	s_nop 0
	v_lshlrev_b32_e32 v14, 16, v232
	v_and_b32_e32 v15, 0xffff0000, v232
	v_lshlrev_b32_e32 v232, 16, v233
	v_and_b32_e32 v233, 0xffff0000, v233
	v_pk_add_f32 v[16:17], v[98:99], v[232:233]
	v_pk_add_f32 v[232:233], v[96:97], v[14:15]
	v_lshlrev_b32_e32 v14, 16, v234
	v_and_b32_e32 v15, 0xffff0000, v234
	v_lshlrev_b32_e32 v234, 16, v235
	v_and_b32_e32 v235, 0xffff0000, v235
	v_pk_add_f32 v[18:19], v[94:95], v[234:235]
	v_pk_add_f32 v[234:235], v[92:93], v[14:15]
	v_cvt_pk_bf16_f32 v232, v232, v233
	v_cvt_pk_bf16_f32 v233, v16, v17
	s_nop 0
	v_cvt_pk_bf16_f32 v234, v234, v235
	v_cvt_pk_bf16_f32 v235, v18, v19
	global_store_dwordx4 v[12:13], v[232:235], off
	s_nop 0
	s_nop 0
	v_lshlrev_b32_e32 v232, 16, v236
	v_and_b32_e32 v233, 0xffff0000, v236
	v_lshlrev_b32_e32 v234, 16, v237
	v_and_b32_e32 v235, 0xffff0000, v237
	v_pk_add_f32 v[234:235], v[90:91], v[234:235]
	v_pk_add_f32 v[232:233], v[88:89], v[232:233]
	v_lshlrev_b32_e32 v236, 16, v238
	v_and_b32_e32 v237, 0xffff0000, v238
	v_lshlrev_b32_e32 v238, 16, v239
	v_and_b32_e32 v239, 0xffff0000, v239
	v_pk_add_f32 v[238:239], v[86:87], v[238:239]
	v_pk_add_f32 v[236:237], v[84:85], v[236:237]
	v_cvt_pk_bf16_f32 v232, v232, v233
	v_cvt_pk_bf16_f32 v233, v234, v235
	s_nop 0
	v_cvt_pk_bf16_f32 v234, v236, v237
	v_cvt_pk_bf16_f32 v235, v238, v239
; __device__ __forceinline__ float bflo(unsigned x) { return __uint_as_float(x << 16); }
; __device__ __forceinline__ float bfhi(unsigned x) { return __uint_as_float(x & 0xffff0000u); }
; __device__ __forceinline__ unsigned cvtpk(float lo, float hi) { unsigned r; asm volatile("v_cvt_pk_bf16_f32 %0, %1, %2" : "=v"(r) : "v"(lo), "v"(hi)); return r; }
;     __device__ __forceinline__ void operator()(const f32x4 (&acc)[2][2][4][2], const Unit& u, int wr, int wc, int fr, int fq) const {
;     ...
;                 for (int m = 0; m < 4; ++m) { const size_t off = (size_t)(row0 + ai * HALF + m * 16) * ldc + col0;
;                     const u32x4 ra = *(const u32x4*)((const bf16_t*)res + off), rb = *(const u32x4*)((const bf16_t*)res + off + HALF);
; #pragma unroll
;                     for (int bj = 0; bj < 2; ++bj) { const u32x4 w_ = bj ? rb : ra; const f32x4 v0 = (f32x4){bflo(w_.x), bfhi(w_.x), bflo(w_.y), bfhi(w_.y)} + acc[ai][bj][m][0], v1 = (f32x4){bflo(w_.z), bfhi(w_.z), bflo(w_.w), bfhi(w_.w)} + acc[ai][bj][m][1];
;                         u32x4 w; w.x = cvtpk(v0[0], v0[1]); w.y = cvtpk(v0[2], v0[3]); w.z = cvtpk(v1[0], v1[1]); w.w = cvtpk(v1[2], v1[3]);
;                         *(u32x4*)(out + off + bj * HALF) = w; }
;                     asm volatile("" ::: "memory"); }
	global_store_dwordx4 v[12:13], v[232:235], off offset:256
	v_lshl_add_u64 v[12:13], v[0:1], 0, s[18:19]
	v_lshl_add_u64 v[8:9], s[62:63], 0, v[12:13]
	s_nop 0
	v_lshl_add_u64 v[12:13], s[6:7], 0, v[12:13]
	s_mov_b64 s[18:19], 0xa0000
	s_nop 0
	v_lshlrev_b32_e32 v14, 16, v240
	v_and_b32_e32 v15, 0xffff0000, v240
	v_lshlrev_b32_e32 v240, 16, v241
	v_and_b32_e32 v241, 0xffff0000, v241
	v_pk_add_f32 v[16:17], v[82:83], v[240:241]
	v_pk_add_f32 v[240:241], v[80:81], v[14:15]
	v_lshlrev_b32_e32 v14, 16, v242
	v_and_b32_e32 v15, 0xffff0000, v242
	v_lshlrev_b32_e32 v242, 16, v243
	v_and_b32_e32 v243, 0xffff0000, v243
	v_pk_add_f32 v[18:19], v[78:79], v[242:243]
	v_pk_add_f32 v[242:243], v[76:77], v[14:15]
	v_cvt_pk_bf16_f32 v240, v240, v241
	v_cvt_pk_bf16_f32 v241, v16, v17
	s_nop 0
	v_cvt_pk_bf16_f32 v242, v242, v243
	v_cvt_pk_bf16_f32 v243, v18, v19
	global_store_dwordx4 v[12:13], v[240:243], off
	s_nop 0
	s_nop 0
	v_lshlrev_b32_e32 v240, 16, v244
	v_and_b32_e32 v241, 0xffff0000, v244
	v_lshlrev_b32_e32 v242, 16, v245
	v_and_b32_e32 v243, 0xffff0000, v245
	v_pk_add_f32 v[242:243], v[74:75], v[242:243]
	v_pk_add_f32 v[240:241], v[72:73], v[240:241]
	v_lshlrev_b32_e32 v244, 16, v246
	v_and_b32_e32 v245, 0xffff0000, v246
	v_lshlrev_b32_e32 v246, 16, v247
	v_and_b32_e32 v247, 0xffff0000, v247
	v_pk_add_f32 v[246:247], v[70:71], v[246:247]
	v_pk_add_f32 v[244:245], v[68:69], v[244:245]
	v_cvt_pk_bf16_f32 v240, v240, v241
	v_cvt_pk_bf16_f32 v241, v242, v243
	s_nop 0
	v_cvt_pk_bf16_f32 v242, v244, v245
	v_cvt_pk_bf16_f32 v243, v246, v247
	global_store_dwordx4 v[12:13], v[240:243], off offset:256
	v_lshl_add_u64 v[12:13], v[0:1], 0, s[18:19]
	v_lshl_add_u64 v[8:9], s[62:63], 0, v[12:13]
	s_nop 0
	v_lshl_add_u64 v[12:13], s[6:7], 0, v[12:13]
	s_mov_b64 s[18:19], 0xb0000
	v_lshl_add_u64 v[0:1], v[0:1], 0, s[18:19]
	s_mov_b64 s[18:19], -1
	s_nop 0
	v_lshlrev_b32_e32 v14, 16, v24
	v_and_b32_e32 v15, 0xffff0000, v24
	v_lshlrev_b32_e32 v24, 16, v25
	v_and_b32_e32 v25, 0xffff0000, v25
	v_pk_add_f32 v[16:17], v[66:67], v[24:25]
	v_pk_add_f32 v[24:25], v[64:65], v[14:15]
	v_lshlrev_b32_e32 v14, 16, v26
	v_and_b32_e32 v15, 0xffff0000, v26
	v_lshlrev_b32_e32 v26, 16, v27
	v_and_b32_e32 v27, 0xffff0000, v27
	v_pk_add_f32 v[18:19], v[62:63], v[26:27]
	v_pk_add_f32 v[26:27], v[60:61], v[14:15]
	v_cvt_pk_bf16_f32 v24, v24, v25
	v_cvt_pk_bf16_f32 v25, v16, v17
	s_nop 0
	v_cvt_pk_bf16_f32 v26, v26, v27
	v_cvt_pk_bf16_f32 v27, v18, v19
	global_store_dwordx4 v[12:13], v[24:27], off
	s_nop 0
	s_nop 0
	v_lshlrev_b32_e32 v24, 16, v28
	v_and_b32_e32 v25, 0xffff0000, v28
	v_lshlrev_b32_e32 v26, 16, v29
	v_and_b32_e32 v27, 0xffff0000, v29
	v_pk_add_f32 v[26:27], v[58:59], v[26:27]
	v_pk_add_f32 v[24:25], v[56:57], v[24:25]
	v_lshlrev_b32_e32 v28, 16, v30
	v_and_b32_e32 v29, 0xffff0000, v30
	v_lshlrev_b32_e32 v30, 16, v31
	v_and_b32_e32 v31, 0xffff0000, v31
	v_pk_add_f32 v[30:31], v[54:55], v[30:31]
	v_pk_add_f32 v[28:29], v[52:53], v[28:29]
	v_cvt_pk_bf16_f32 v24, v24, v25
	v_cvt_pk_bf16_f32 v25, v26, v27
	s_nop 0
	v_cvt_pk_bf16_f32 v26, v28, v29
	v_cvt_pk_bf16_f32 v27, v30, v31
	global_store_dwordx4 v[12:13], v[24:27], off offset:256
	v_lshl_add_u64 v[8:9], s[62:63], 0, v[0:1]
	s_nop 0
	v_lshl_add_u64 v[0:1], s[6:7], 0, v[0:1]
	s_nop 0
	v_lshlrev_b32_e32 v12, 16, v196
	v_and_b32_e32 v13, 0xffff0000, v196
	v_lshlrev_b32_e32 v196, 16, v197
	v_and_b32_e32 v197, 0xffff0000, v197
	v_pk_add_f32 v[14:15], v[50:51], v[196:197]
	v_pk_add_f32 v[196:197], v[48:49], v[12:13]
	v_lshlrev_b32_e32 v12, 16, v198
	v_and_b32_e32 v13, 0xffff0000, v198
	v_lshlrev_b32_e32 v198, 16, v199
	v_and_b32_e32 v199, 0xffff0000, v199
	v_pk_add_f32 v[16:17], v[46:47], v[198:199]
	v_pk_add_f32 v[198:199], v[44:45], v[12:13]
	v_cvt_pk_bf16_f32 v196, v196, v197
	v_cvt_pk_bf16_f32 v197, v14, v15
	s_nop 0
	v_cvt_pk_bf16_f32 v198, v198, v199
	v_cvt_pk_bf16_f32 v199, v16, v17
	global_store_dwordx4 v[0:1], v[196:199], off
	s_nop 0
	s_nop 0
	v_lshlrev_b32_e32 v196, 16, v180
	v_and_b32_e32 v197, 0xffff0000, v180
	v_lshlrev_b32_e32 v198, 16, v181
	v_and_b32_e32 v199, 0xffff0000, v181
	v_pk_add_f32 v[198:199], v[42:43], v[198:199]
	v_pk_add_f32 v[196:197], v[40:41], v[196:197]
	v_lshlrev_b32_e32 v180, 16, v182
	v_and_b32_e32 v181, 0xffff0000, v182
	v_lshlrev_b32_e32 v182, 16, v183
	v_and_b32_e32 v183, 0xffff0000, v183
	v_pk_add_f32 v[182:183], v[38:39], v[182:183]
	v_pk_add_f32 v[180:181], v[36:37], v[180:181]
	v_cvt_pk_bf16_f32 v196, v196, v197
	v_cvt_pk_bf16_f32 v197, v198, v199
	s_nop 0
	v_cvt_pk_bf16_f32 v198, v180, v181
	v_cvt_pk_bf16_f32 v199, v182, v183
	global_store_dwordx4 v[0:1], v[196:199], off offset:256
	s_cbranch_vccnz .LBB0_2578
	s_andn2_b64 vcc, exec, s[4:5]
	s_cbranch_vccnz .LBB0_2577
	s_barrier
	s_branch .LBB0_2577

; __global__ void __launch_bounds__(512, 2) fwd(Args args) {
	.amdhsa_kernel _Z3fwd4Args
		.amdhsa_group_segment_fixed_size 0
		.amdhsa_private_segment_fixed_size 0
		.amdhsa_kernarg_size 464
		.amdhsa_user_sgpr_count 2
		.amdhsa_user_sgpr_dispatch_ptr 0
		.amdhsa_user_sgpr_queue_ptr 0
		.amdhsa_user_sgpr_kernarg_segment_ptr 1
		.amdhsa_user_sgpr_dispatch_id 0
		.amdhsa_user_sgpr_kernarg_preload_length 0
		.amdhsa_user_sgpr_kernarg_preload_offset 0
		.amdhsa_user_sgpr_private_segment_size 0
		.amdhsa_uses_dynamic_stack 0
		.amdhsa_enable_private_segment 0
		.amdhsa_system_sgpr_workgroup_id_x 1
		.amdhsa_system_sgpr_workgroup_id_y 0
		.amdhsa_system_sgpr_workgroup_id_z 0
		.amdhsa_system_sgpr_workgroup_info 0
		.amdhsa_system_vgpr_workitem_id 0
		.amdhsa_next_free_vgpr 256
		.amdhsa_next_free_sgpr 102
		.amdhsa_accum_offset 256
		.amdhsa_reserve_vcc 1
		.amdhsa_float_round_mode_32 0
		.amdhsa_float_round_mode_16_64 0
		.amdhsa_float_denorm_mode_32 3
		.amdhsa_float_denorm_mode_16_64 3
		.amdhsa_dx10_clamp 1
		.amdhsa_ieee_mode 1
		.amdhsa_fp16_overflow 0
		.amdhsa_tg_split 0
		.amdhsa_exception_fp_ieee_invalid_op 0
		.amdhsa_exception_fp_denorm_src 0
		.amdhsa_exception_fp_ieee_div_zero 0
		.amdhsa_exception_fp_ieee_overflow 0
		.amdhsa_exception_fp_ieee_underflow 0
		.amdhsa_exception_fp_ieee_inexact 0
		.amdhsa_exception_int_div_zero 0
	.end_amdhsa_kernel

; __global__ void __launch_bounds__(512, 2) fwd(Args args) {
amdhsa.kernels:
  - .agpr_count:     0
    .args:
      - .offset:         0
        .size:           208
        .value_kind:     by_value
      - .offset:         208
        .size:           4
        .value_kind:     hidden_block_count_x
      - .offset:         212
        .size:           4
        .value_kind:     hidden_block_count_y
      - .offset:         216
        .size:           4
        .value_kind:     hidden_block_count_z
      - .offset:         220
        .size:           2
        .value_kind:     hidden_group_size_x
      - .offset:         222
        .size:           2
        .value_kind:     hidden_group_size_y
      - .offset:         224
        .size:           2
        .value_kind:     hidden_group_size_z
      - .offset:         226
        .size:           2
        .value_kind:     hidden_remainder_x
      - .offset:         228
        .size:           2
        .value_kind:     hidden_remainder_y
      - .offset:         230
        .size:           2
        .value_kind:     hidden_remainder_z
      - .offset:         248
        .size:           8
        .value_kind:     hidden_global_offset_x
      - .offset:         256
        .size:           8
        .value_kind:     hidden_global_offset_y
      - .offset:         264
        .size:           8
        .value_kind:     hidden_global_offset_z
      - .offset:         272
        .size:           2
        .value_kind:     hidden_grid_dims
      - .offset:         328
        .size:           4
        .value_kind:     hidden_dynamic_lds_size
    .group_segment_fixed_size: 0
    .kernarg_segment_align: 8
    .kernarg_segment_size: 464
    .language:       OpenCL C
    .language_version:
      - 2
      - 0
    .max_flat_workgroup_size: 512
    .name:           _Z3fwd4Args
    .private_segment_fixed_size: 0
    .sgpr_count:     108
    .sgpr_spill_count: 384
    .symbol:         _Z3fwd4Args.kd
    .uniform_work_group_size: 1
    .uses_dynamic_stack: false
    .vgpr_count:     256
    .vgpr_spill_count: 0
    .wavefront_size: 64
